# speedup vs baseline: 1.0384x; 1.0265x over previous
_Z5k_decPKiPKDF16_S2_PKfS4_S4_Pf:
	s_load_dword s3, s[0:1], 0x44
	s_load_dword s6, s[0:1], 0x38
	s_load_dwordx2 s[4:5], s[0:1], 0x0
	s_load_dwordx8 s[28:35], s[0:1], 0x8
	s_load_dwordx4 s[12:15], s[0:1], 0x28
	v_and_b32_e32 v1, 15, v0
	v_and_b32_e32 v64, 63, v0
	v_lshlrev_b32_e32 v96, 3, v1
	v_lshrrev_b32_e32 v4, 3, v0
	v_and_b32_e32 v4, 4, v4
	v_or_b32_e32 v96, v96, v4
	v_mov_b32_e32 v97, 0
	v_and_b32_e32 v104, 16, v0
	v_lshlrev_b32_e32 v6, 7, v0
	v_lshlrev_b32_e32 v7, 2, v64
	s_movk_i32 s16, 0x6000
	v_and_or_b32 v103, v6, s16, v7
	v_mov_b32_e32 v219, 0
	s_movk_i32 s19, 0x3d08
	s_waitcnt lgkmcnt(0)
	s_and_b32 s3, s3, 0xffff
	s_mul_i32 s2, s2, s3
	v_add_u32_e32 v5, s2, v0
	s_mul_i32 s6, s6, s3
	v_lshrrev_b32_e32 v102, 6, v5
	s_lshr_b32 s18, s6, 6
	v_lshl_add_u64 v[2:3], s[4:5], 0, v[96:97]
	s_mov_b32 s16, 0xf4240
	v_cmp_gt_u32_e32 vcc, s16, v5
	s_and_saveexec_b64 s[22:23], vcc
	s_cbranch_execz .LBB2_3
	v_mov_b32_e32 v222, v2
	v_mov_b32_e32 v223, v3
	v_min_u32_e32 v218, s19, v102
	v_lshlrev_b32_e32 v218, 9, v218
	v_lshl_add_u64 v[216:217], v[222:223], 0, v[218:219]
	global_load_dword v65, v[216:217], off nt
	global_load_dword v80, v[216:217], off offset:128 nt
	global_load_dword v81, v[216:217], off offset:256 nt
	global_load_dword v82, v[216:217], off offset:384 nt
	v_add_u32_e32 v220, s18, v102
	v_min_u32_e32 v218, s19, v220
	v_lshlrev_b32_e32 v218, 9, v218
	v_lshl_add_u64 v[216:217], v[222:223], 0, v[218:219]
	global_load_dword v100, v[216:217], off nt
	global_load_dword v101, v[216:217], off offset:128 nt
	global_load_dword v98, v[216:217], off offset:256 nt
	global_load_dword v99, v[216:217], off offset:384 nt
	s_mov_b32 s8, s28
	s_and_b32 s9, s29, 0xffff
	s_mov_b32 s10, 0x30d400
	s_mov_b32 s11, 0x20000
	s_mov_b64 s[36:37], 0x1000
	v_and_b32_e32 v96, 48, v64
	v_lshlrev_b32_e32 v221, 6, v1
	v_mov_b32_e32 v214, v221
	v_mov_b32_e32 v215, 0
	v_lshl_add_u64 v[216:217], s[30:31], 0, v[96:97]
	v_lshl_add_u64 v[48:49], v[216:217], 0, v[214:215]
	v_lshl_add_u64 v[66:67], v[48:49], 0, s[36:37]
	v_lshl_or_b32 v221, v102, 6, v64
	v_lshrrev_b32_e32 v213, 4, v64
	v_cmp_gt_u32_e32 vcc, 16, v64
	global_load_dwordx4 v[68:71], v96, s[34:35]
	global_load_dwordx4 v[0:3], v96, s[32:33]
	global_load_dwordx4 v[72:75], v96, s[34:35] offset:64
	global_load_dwordx4 v[4:7], v96, s[32:33] offset:64
	global_load_dwordx4 v[76:79], v96, s[34:35] offset:128
	global_load_dwordx4 v[8:11], v96, s[32:33] offset:128
	global_load_dwordx4 v[106:109], v96, s[34:35] offset:192
	global_load_dwordx4 v[12:15], v96, s[32:33] offset:192
	global_load_dwordx4 v[110:113], v96, s[34:35] offset:256
	global_load_dwordx4 v[16:19], v96, s[32:33] offset:256
	global_load_dwordx4 v[114:117], v96, s[34:35] offset:320
	global_load_dwordx4 v[20:23], v96, s[32:33] offset:320
	global_load_dwordx4 v[118:121], v96, s[34:35] offset:384
	global_load_dwordx4 v[24:27], v96, s[32:33] offset:384
	global_load_dwordx4 v[122:125], v96, s[34:35] offset:448
	global_load_dwordx4 v[28:31], v96, s[32:33] offset:448
	global_load_dwordx4 v[32:35], v[48:49], off
	global_load_dwordx4 v[36:39], v[48:49], off offset:1024
	global_load_dwordx4 v[40:43], v[48:49], off offset:2048
	global_load_dwordx4 v[44:47], v[48:49], off offset:3072
	s_nop 0
	global_load_dwordx4 v[48:51], v[66:67], off
	global_load_dwordx4 v[52:55], v[66:67], off offset:1024
	global_load_dwordx4 v[56:59], v[66:67], off offset:2048
	global_load_dwordx4 v[60:63], v[66:67], off offset:3072
	s_load_dword s12, s[12:13], 0x0
	s_waitcnt vmcnt(28)
	v_lshl_or_b32 v216, v65, 5, v104
	v_lshl_or_b32 v217, v80, 5, v104
	v_lshl_or_b32 v218, v81, 5, v104
	v_lshl_or_b32 v212, v82, 5, v104
	buffer_load_dwordx4 v[92:95], v216, s[8:11], 0 offen
	buffer_load_dwordx4 v[88:91], v217, s[8:11], 0 offen
	buffer_load_dwordx4 v[84:87], v218, s[8:11], 0 offen
	buffer_load_dwordx4 v[80:83], v212, s[8:11], 0 offen
	v_add_u32_e32 v220, s18, v102
	v_add_u32_e32 v220, s18, v220
	v_min_u32_e32 v218, s19, v220
	v_lshlrev_b32_e32 v218, 9, v218
	v_lshl_add_u64 v[216:217], v[222:223], 0, v[218:219]
	global_load_dword v224, v[216:217], off nt
	global_load_dword v225, v[216:217], off offset:128 nt
	global_load_dword v226, v[216:217], off offset:256 nt
	global_load_dword v227, v[216:217], off offset:384 nt
	v_add_u32_e32 v220, s18, v220
	v_min_u32_e32 v218, s19, v220
	v_lshlrev_b32_e32 v218, 9, v218
	v_lshl_add_u64 v[216:217], v[222:223], 0, v[218:219]
	global_load_dword v228, v[216:217], off nt
	global_load_dword v229, v[216:217], off offset:128 nt
	global_load_dword v230, v[216:217], off offset:256 nt
	global_load_dword v231, v[216:217], off offset:384 nt
	v_add_u32_e32 v220, s18, v220
	v_min_u32_e32 v218, s19, v220
	v_lshlrev_b32_e32 v218, 9, v218
	v_lshl_add_u64 v[216:217], v[222:223], 0, v[218:219]
	global_load_dword v232, v[216:217], off nt
	global_load_dword v233, v[216:217], off offset:128 nt
	global_load_dword v234, v[216:217], off offset:256 nt
	global_load_dword v235, v[216:217], off offset:384 nt
	v_add_u32_e32 v220, s18, v220
	v_min_u32_e32 v218, s19, v220
	v_lshlrev_b32_e32 v218, 9, v218
	v_lshl_add_u64 v[216:217], v[222:223], 0, v[218:219]
	global_load_dword v236, v[216:217], off nt
	global_load_dword v237, v[216:217], off offset:128 nt
	global_load_dword v238, v[216:217], off offset:256 nt
	global_load_dword v239, v[216:217], off offset:384 nt
	v_add_u32_e32 v220, s18, v220
	v_min_u32_e32 v218, s19, v220
	v_lshlrev_b32_e32 v218, 9, v218
	v_lshl_add_u64 v[216:217], v[222:223], 0, v[218:219]
	global_load_dword v240, v[216:217], off nt
	global_load_dword v241, v[216:217], off offset:128 nt
	global_load_dword v242, v[216:217], off offset:256 nt
	global_load_dword v243, v[216:217], off offset:384 nt
	v_add_u32_e32 v220, s18, v220
	v_min_u32_e32 v218, s19, v220
	v_lshlrev_b32_e32 v218, 9, v218
	v_lshl_add_u64 v[216:217], v[222:223], 0, v[218:219]
	global_load_dword v244, v[216:217], off nt
	global_load_dword v245, v[216:217], off offset:128 nt
	global_load_dword v246, v[216:217], off offset:256 nt
	global_load_dword v247, v[216:217], off offset:384 nt
	s_lshl_b32 s21, s18, 6
	s_mov_b32 s20, 2
	s_mov_b64 s[16:17], 0
	v_cmp_eq_u32_e64 s[0:1], 1, v213
	v_cmp_eq_u32_e64 s[2:3], 2, v213
	v_cmp_eq_u32_e64 s[4:5], 3, v213
	v_mov_b32_e32 v96, v221
	v_mov_b32_e32 v97, 0
	s_waitcnt vmcnt(28)
	v_cvt_pk_f16_f32 v67, v74, v75
	v_cvt_pk_f16_f32 v66, v72, v73
	v_cvt_pk_f16_f32 v65, v70, v71
	v_cvt_pk_f16_f32 v64, v68, v69
	v_cvt_pk_f16_f32 v71, v108, v109
	v_cvt_pk_f16_f32 v70, v106, v107
	v_cvt_pk_f16_f32 v69, v78, v79
	v_cvt_pk_f16_f32 v68, v76, v77
	v_cvt_pk_f16_f32 v75, v116, v117
	v_cvt_pk_f16_f32 v74, v114, v115
	v_cvt_pk_f16_f32 v73, v112, v113
	v_cvt_pk_f16_f32 v72, v110, v111
	v_cvt_pk_f16_f32 v79, v124, v125
	v_cvt_pk_f16_f32 v78, v122, v123
	v_cvt_pk_f16_f32 v77, v120, v121
	v_cvt_pk_f16_f32 v76, v118, v119
	s_waitcnt vmcnt(24)
.LBB2_2:
	s_nop 0
	v_mfma_f32_16x16x32_f16 v[110:113], v[36:39], v[92:95], v[4:7]
	s_min_i32 s6, s20, 7
	v_add_u32_e32 v102, s18, v102
	s_add_i32 s20, s20, 1
	v_mfma_f32_16x16x32_f16 v[106:109], v[32:35], v[92:95], v[0:3]
	s_nop 0
	v_mfma_f32_16x16x32_f16 v[122:125], v[32:35], v[88:91], v[0:3]
	s_nop 1
	v_cvt_pk_f16_f32 v163, v110, v111
	v_cvt_pk_f16_f32 v164, v112, v113
	s_nop 1
	v_cvt_pk_f16_f32 v105, v106, v107
	v_mfma_f32_16x16x32_f16 v[134:137], v[44:47], v[88:91], v[12:15]
	v_cvt_pk_f16_f32 v162, v108, v109
	v_cvt_pk_f16_f32 v169, v122, v123
	v_cvt_pk_f16_f32 v170, v124, v125
	s_nop 0
	v_mfma_f32_16x16x32_f16 v[138:141], v[32:35], v[84:87], v[0:3]
	v_mfma_f32_16x16x32_f16 v[142:145], v[36:39], v[84:87], v[4:7]
	s_nop 1
	v_cvt_pk_f16_f32 v136, v136, v137
	s_nop 3
	v_cvt_pk_f16_f32 v137, v138, v139
	v_cvt_pk_f16_f32 v138, v140, v141
	v_mfma_f32_16x16x32_f16 v[150:153], v[44:47], v[84:87], v[12:15]
	v_cvt_pk_f16_f32 v175, v134, v135
	v_cvt_pk_f16_f32 v139, v142, v143
	v_cvt_pk_f16_f32 v140, v144, v145
	s_nop 0
	v_mfma_f32_16x16x32_f16 v[110:113], v[44:47], v[80:83], v[12:15]
	v_lshl_add_u64 v[134:135], v[96:97], 2, s[14:15]
	s_nop 1
	v_cvt_pk_f16_f32 v143, v150, v151
	v_cvt_pk_f16_f32 v144, v152, v153
	v_mfma_f32_16x16x32_f16 v[118:121], v[44:47], v[92:95], v[12:15]
	v_add_u32_e32 v96, s21, v96
	s_nop 0
	v_cvt_pk_f16_f32 v151, v110, v111
	v_cvt_pk_f16_f32 v152, v112, v113
	v_mfma_f32_16x16x32_f16 v[130:133], v[40:43], v[88:91], v[8:11]
	v_mfma_f32_16x16x32_f16 v[146:149], v[40:43], v[84:87], v[8:11]
	s_nop 1
	v_cvt_pk_f16_f32 v167, v118, v119
	v_cvt_pk_f16_f32 v168, v120, v121
	s_nop 2
	v_cvt_pk_f16_f32 v173, v130, v131
	v_mfma_f32_16x16x32_f16 v[154:157], v[32:35], v[80:83], v[0:3]
	v_cvt_pk_f16_f32 v174, v132, v133
	v_cvt_pk_f16_f32 v141, v146, v147
	v_cvt_pk_f16_f32 v142, v148, v149
	v_mfma_f32_16x16x32_f16 v[158:161], v[36:39], v[80:83], v[4:7]
	v_mfma_f32_16x16x32_f16 v[106:109], v[40:43], v[80:83], v[8:11]
	s_nop 2
	v_cvt_pk_f16_f32 v146, v156, v157
	s_nop 2
	v_cvt_pk_f16_f32 v147, v158, v159
	v_cvt_pk_f16_f32 v145, v154, v155
	v_mfma_f32_16x16x32_f16 v[122:125], v[48:51], v[88:91], v[16:19]
	v_cvt_pk_f16_f32 v148, v160, v161
	v_cvt_pk_f16_f32 v149, v106, v107
	v_cvt_pk_f16_f32 v150, v108, v109
	v_mfma_f32_16x16x32_f16 v[110:113], v[48:51], v[80:83], v[16:19]
	v_mfma_f32_16x16x32_f16 v[114:117], v[40:43], v[92:95], v[8:11]
	s_nop 2
	v_cvt_pk_f16_f32 v157, v122, v123
	v_cvt_pk_f16_f32 v158, v124, v125
	v_lshl_or_b32 v122, v100, 5, v104
	v_mfma_f32_16x16x32_f16 v[118:121], v[52:55], v[92:95], v[20:23]
	v_lshl_or_b32 v123, v101, 5, v104
	v_cvt_pk_f16_f32 v179, v110, v111
	v_lshl_or_b32 v124, v98, 5, v104
	v_mfma_f32_16x16x32_f16 v[130:133], v[48:51], v[84:87], v[16:19]
	v_lshl_or_b32 v110, v99, 5, v104
	v_cvt_pk_f16_f32 v165, v114, v115
	v_cvt_pk_f16_f32 v166, v116, v117
	v_mfma_f32_16x16x32_f16 v[106:109], v[52:55], v[84:87], v[20:23]
	v_cvt_pk_f16_f32 v155, v118, v119
	v_cvt_pk_f16_f32 v156, v120, v121
	v_cvt_pk_f16_f32 v180, v112, v113
	v_mfma_f32_16x16x32_f16 v[98:101], v[56:59], v[84:87], v[24:27]
	v_pk_max_f16 v111, v138, 0
	s_nop 2
	v_cvt_pk_f16_f32 v177, v106, v107
	v_cvt_pk_f16_f32 v178, v108, v109
	v_mfma_f32_16x16x32_f16 v[84:87], v[60:63], v[84:87], v[28:31]
	v_pk_max_f16 v112, v139, 0
	v_cvt_pk_f16_f32 v191, v98, v99
	v_cvt_pk_f16_f32 v192, v100, v101
	v_mfma_f32_16x16x32_f16 v[114:117], v[48:51], v[92:95], v[16:19]
	v_pk_max_f16 v98, v169, 0
	s_nop 2
	v_cvt_pk_f16_f32 v193, v84, v85
	v_cvt_pk_f16_f32 v194, v86, v87
	v_mfma_f32_16x16x32_f16 v[118:121], v[56:59], v[92:95], v[24:27]
	buffer_load_dwordx4 v[84:87], v110, s[8:11], 0 offen
	v_cvt_pk_f16_f32 v153, v114, v115
	v_cvt_pk_f16_f32 v154, v116, v117
	v_mfma_f32_16x16x32_f16 v[92:95], v[60:63], v[92:95], v[28:31]
	v_pk_max_f16 v99, v170, 0
	s_nop 2
	v_cvt_pk_f16_f32 v183, v118, v119
	v_cvt_pk_f16_f32 v184, v120, v121
	buffer_load_dwordx4 v[118:121], v123, s[8:11], 0 offen
	v_mfma_f32_16x16x32_f16 v[126:129], v[36:39], v[88:91], v[4:7]
	v_cvt_pk_f16_f32 v185, v92, v93
	v_cvt_pk_f16_f32 v186, v94, v95
	buffer_load_dwordx4 v[92:95], v122, s[8:11], 0 offen
	v_mfma_f32_16x16x32_f16 v[106:109], v[56:59], v[88:91], v[24:27]
	buffer_load_dwordx4 v[122:125], v124, s[8:11], 0 offen
	s_nop 2
	v_cvt_pk_f16_f32 v171, v126, v127
	v_cvt_pk_f16_f32 v172, v128, v129
	v_mfma_f32_16x16x32_f16 v[126:129], v[52:55], v[88:91], v[20:23]
	v_pk_max_f16 v100, v171, 0
	v_pk_max_f16 v101, v172, 0
	v_pk_max_f16 v110, v137, 0
	v_mfma_f32_16x16x32_f16 v[88:91], v[60:63], v[88:91], v[28:31]
	v_pk_max_f16 v113, v140, 0
	v_cvt_pk_f16_f32 v187, v106, v107
	v_cvt_pk_f16_f32 v188, v108, v109
	v_mfma_f32_16x16x32_f16 v[114:117], v[52:55], v[80:83], v[20:23]
	v_pk_max_f16 v106, v173, 0
	s_nop 2
	v_cvt_pk_f16_f32 v189, v88, v89
	v_cvt_pk_f16_f32 v190, v90, v91
	v_mfma_f32_16x16x32_f16 v[88:91], v[56:59], v[80:83], v[24:27]
	v_pk_max_f16 v107, v174, 0
	v_pk_max_f16 v108, v175, 0
	v_pk_max_f16 v109, v136, 0
	v_mfma_f32_16x16x32_f16 v[80:83], v[60:63], v[80:83], v[28:31]
	v_cvt_pk_f16_f32 v181, v114, v115
	s_nop 2
	v_cvt_pk_f16_f32 v195, v88, v89
	v_cvt_pk_f16_f32 v196, v90, v91
	v_pk_max_f16 v88, v165, 0
	v_pk_max_f16 v89, v166, 0
	v_cvt_pk_f16_f32 v197, v80, v81
	v_cvt_pk_f16_f32 v198, v82, v83
	v_pk_max_f16 v80, v105, 0
	v_pk_max_f16 v81, v162, 0
	v_pk_max_f16 v82, v163, 0
	v_pk_max_f16 v83, v164, 0
	v_pk_max_f16 v90, v167, 0
	v_pk_max_f16 v91, v168, 0
	v_mfma_f32_16x16x32_f16 v[80:83], v[64:67], v[80:83], 0
	v_cvt_pk_f16_f32 v182, v116, v117
	v_pk_max_f16 v114, v141, 0
	v_pk_max_f16 v115, v142, 0
	v_mfma_f32_16x16x32_f16 v[98:101], v[64:67], v[98:101], 0
	v_pk_max_f16 v116, v143, 0
	v_pk_max_f16 v117, v144, 0
	v_cvt_pk_f16_f32 v159, v126, v127
	v_mfma_f32_16x16x32_f16 v[80:83], v[68:71], v[88:91], v[80:83]
	v_pk_max_f16 v88, v145, 0
	v_pk_max_f16 v89, v146, 0
	v_pk_max_f16 v90, v147, 0
	v_pk_max_f16 v91, v148, 0
	v_mfma_f32_16x16x32_f16 v[110:113], v[64:67], v[110:113], 0
	v_cvt_pk_f16_f32 v160, v128, v129
	v_pk_max_f16 v126, v149, 0
	v_pk_max_f16 v127, v150, 0
	v_mfma_f32_16x16x32_f16 v[88:91], v[64:67], v[88:91], 0
	v_pk_max_f16 v128, v151, 0
	v_pk_max_f16 v129, v152, 0
	v_cvt_pk_f16_f32 v161, v130, v131
	v_mfma_f32_16x16x32_f16 v[106:109], v[68:71], v[106:109], v[98:101]
	v_cvt_pk_f16_f32 v176, v132, v133
	v_pk_max_f16 v130, v157, 0
	v_pk_max_f16 v131, v158, 0
	v_mfma_f32_16x16x32_f16 v[110:113], v[68:71], v[114:117], v[110:113]
	v_pk_max_f16 v114, v153, 0
	v_pk_max_f16 v115, v154, 0
	v_pk_max_f16 v116, v155, 0
	v_pk_max_f16 v117, v156, 0
	v_mfma_f32_16x16x32_f16 v[88:91], v[68:71], v[126:129], v[88:91]
	v_pk_max_f16 v132, v159, 0
	v_pk_max_f16 v133, v160, 0
	v_pk_max_f16 v126, v161, 0
	v_mfma_f32_16x16x32_f16 v[80:83], v[72:75], v[114:117], v[80:83]
	v_pk_max_f16 v127, v176, 0
	v_pk_max_f16 v128, v177, 0
	v_pk_max_f16 v129, v178, 0
	v_mfma_f32_16x16x32_f16 v[106:109], v[72:75], v[130:133], v[106:109]
	v_pk_max_f16 v114, v179, 0
	v_pk_max_f16 v115, v180, 0
	v_pk_max_f16 v116, v181, 0
	v_pk_max_f16 v117, v182, 0
	v_mfma_f32_16x16x32_f16 v[110:113], v[72:75], v[126:129], v[110:113]
	v_pk_max_f16 v130, v183, 0
	v_pk_max_f16 v131, v184, 0
	v_pk_max_f16 v132, v185, 0
	v_pk_max_f16 v133, v186, 0
	v_mfma_f32_16x16x32_f16 v[88:91], v[72:75], v[114:117], v[88:91]
	v_pk_max_f16 v114, v187, 0
	v_pk_max_f16 v115, v188, 0
	v_pk_max_f16 v116, v189, 0
	v_mfma_f32_16x16x32_f16 v[80:83], v[76:79], v[130:133], v[80:83]
	v_pk_max_f16 v117, v190, 0
	v_pk_max_f16 v126, v191, 0
	v_pk_max_f16 v127, v192, 0
	v_mfma_f32_16x16x32_f16 v[106:109], v[76:79], v[114:117], v[106:109]
	v_pk_max_f16 v128, v193, 0
	v_pk_max_f16 v129, v194, 0
	s_nop 1
	v_cndmask_b32_e32 v80, 0, v80, vcc
	v_lshl_add_u32 v105, s6, 10, v103
	v_mfma_f32_16x16x32_f16 v[112:115], v[76:79], v[126:129], v[110:113]
	s_nop 0
	v_pk_max_f16 v108, v195, 0
	v_pk_max_f16 v109, v196, 0
	v_cndmask_b32_e64 v80, v80, v106, s[0:1]
	v_pk_max_f16 v110, v197, 0
	v_pk_max_f16 v111, v198, 0
	s_nop 1
	v_cndmask_b32_e64 v80, v80, v112, s[2:3]
	s_cmp_lg_u32 s20, 3
	s_cbranch_scc1 .Ldec_noidx
	s_waitcnt vmcnt(4)
	ds_write2st64_b32 v103, v224, v225 offset0:8 offset1:9
	ds_write2st64_b32 v103, v226, v227 offset0:10 offset1:11
	ds_write2st64_b32 v103, v228, v229 offset0:12 offset1:13
	ds_write2st64_b32 v103, v230, v231 offset0:14 offset1:15
	ds_write2st64_b32 v103, v232, v233 offset0:16 offset1:17
	ds_write2st64_b32 v103, v234, v235 offset0:18 offset1:19
	ds_write2st64_b32 v103, v236, v237 offset0:20 offset1:21
	ds_write2st64_b32 v103, v238, v239 offset0:22 offset1:23
	ds_write2st64_b32 v103, v240, v241 offset0:24 offset1:25
	ds_write2st64_b32 v103, v242, v243 offset0:26 offset1:27
	ds_write2st64_b32 v103, v244, v245 offset0:28 offset1:29
	ds_write2st64_b32 v103, v246, v247 offset0:30 offset1:31
.Ldec_noidx:
	ds_read2st64_b32 v[100:101], v105 offset1:1
	ds_read2st64_b32 v[98:99], v105 offset0:2 offset1:3
	v_mfma_f32_16x16x32_f16 v[88:91], v[76:79], v[108:111], v[88:91]
	v_cmp_lt_u32_e64 s[6:7], s19, v102
	s_or_b64 s[16:17], s[6:7], s[16:17]
	s_nop 5
	v_cndmask_b32_e64 v80, v80, v88, s[4:5]
	s_waitcnt lgkmcnt(0)
	v_add_f32_e32 v80, s12, v80
	v_mul_f32_e32 v80, 0xbfb8aa3b, v80
	v_exp_f32_e32 v80, v80
	s_waitcnt vmcnt(2)
	v_mov_b32_e32 v88, v118
	v_mov_b32_e32 v89, v119
	v_mov_b32_e32 v90, v120
	v_add_f32_e32 v80, 1.0, v80
	v_rcp_f32_e32 v80, v80
	v_mov_b32_e32 v91, v121
	global_store_dword v[134:135], v80, off
	v_mov_b64_e32 v[80:81], v[84:85]
	v_mov_b64_e32 v[82:83], v[86:87]
	s_waitcnt vmcnt(1)
	v_mov_b32_e32 v84, v122
	v_mov_b32_e32 v85, v123
	v_mov_b32_e32 v86, v124
	v_mov_b32_e32 v87, v125
	s_andn2_b64 exec, exec, s[16:17]
	s_cbranch_execnz .LBB2_2

	.amdhsa_kernel _Z5k_decPKiPKDF16_S2_PKfS4_S4_Pf
		.amdhsa_group_segment_fixed_size 32768
		.amdhsa_private_segment_fixed_size 0
		.amdhsa_kernarg_size 312
		.amdhsa_user_sgpr_count 2
		.amdhsa_user_sgpr_dispatch_ptr 0
		.amdhsa_user_sgpr_queue_ptr 0
		.amdhsa_user_sgpr_kernarg_segment_ptr 1
		.amdhsa_user_sgpr_dispatch_id 0
		.amdhsa_user_sgpr_kernarg_preload_length 0
		.amdhsa_user_sgpr_kernarg_preload_offset 0
		.amdhsa_user_sgpr_private_segment_size 0
		.amdhsa_uses_dynamic_stack 0
		.amdhsa_enable_private_segment 0
		.amdhsa_system_sgpr_workgroup_id_x 1
		.amdhsa_system_sgpr_workgroup_id_y 0
		.amdhsa_system_sgpr_workgroup_id_z 0
		.amdhsa_system_sgpr_workgroup_info 0
		.amdhsa_system_vgpr_workitem_id 0
		.amdhsa_next_free_vgpr 248
		.amdhsa_next_free_sgpr 96
		.amdhsa_accum_offset 248
		.amdhsa_reserve_vcc 1
		.amdhsa_float_round_mode_32 0
		.amdhsa_float_round_mode_16_64 0
		.amdhsa_float_denorm_mode_32 3
		.amdhsa_float_denorm_mode_16_64 3
		.amdhsa_dx10_clamp 1
		.amdhsa_ieee_mode 1
		.amdhsa_fp16_overflow 0
		.amdhsa_tg_split 0
		.amdhsa_exception_fp_ieee_invalid_op 0
		.amdhsa_exception_fp_denorm_src 0
		.amdhsa_exception_fp_ieee_div_zero 0
		.amdhsa_exception_fp_ieee_overflow 0
		.amdhsa_exception_fp_ieee_underflow 0
		.amdhsa_exception_fp_ieee_inexact 0
		.amdhsa_exception_int_div_zero 0
	.end_amdhsa_kernel

_Z5k_aggILi1EEvPKiS1_S1_PKDv4_jPKfS6_PS2_PDF16_:
	s_load_dwordx8 s[4:11], s[0:1], 0x0
	s_load_dwordx4 s[16:19], s[0:1], 0x20
	s_load_dwordx2 s[20:21], s[0:1], 0x30
	s_and_b32 s0, s2, 7
	s_mulk_i32 s0, 0x30e
	s_lshr_b32 s1, s2, 3
	s_add_i32 s0, s0, s1
	v_lshl_or_b32 v1, s0, 6, v0
	v_ashrrev_i32_e32 v1, 2, v1
	s_mov_b32 s0, 0x186a0
	v_mov_b32_e32 v2, 0x1869f
	v_cmp_gt_i32_e32 vcc, s0, v1
	v_and_b32_e32 v28, 3, v0
	s_nop 0
	v_cndmask_b32_e32 v26, v2, v1, vcc
	v_ashrrev_i32_e32 v27, 31, v26
	v_lshlrev_b64 v[2:3], 2, v[26:27]
	s_waitcnt lgkmcnt(0)
	s_load_dwordx16 s[60:75], s[18:19], 0x0
	v_lshl_add_u64 v[4:5], s[4:5], 0, v[2:3]
	global_load_dword v16, v[4:5], off
	v_lshl_add_u64 v[4:5], s[6:7], 0, v[2:3]
	global_load_dword v1, v[4:5], off
	s_mov_b32 s7, 0x20000
	s_mov_b32 s6, 0x186a00
	s_and_b32 s5, s11, 0xffff
	s_mov_b32 s4, s10
	v_lshlrev_b32_e32 v4, 4, v26
	v_lshl_add_u64 v[2:3], s[16:17], 0, v[2:3]
	buffer_load_dwordx4 v[18:21], v4, s[4:7], 0 offen
	global_load_dword v30, v[2:3], off
	s_waitcnt vmcnt(2)
	v_cndmask_b32_e32 v31, v16, v1, vcc
	v_add_u32_e32 v22, v16, v28
	s_mov_b32 s24, s8
	s_and_b32 s25, s9, 0xffff
	s_mov_b32 s26, 0x7fffffff
	s_mov_b32 s27, 0x20000
	v_sub_u32_e32 v23, v31, v22
	v_lshlrev_b32_e32 v22, 2, v22
	v_mov_b32_e32 v29, 0x7ffffff0
	v_mov_b32_e32 v0, 0
	v_mov_b32_e32 v1, v0
	v_mov_b32_e32 v2, v0
	v_mov_b32_e32 v3, v0
	v_mov_b32_e32 v4, v0
	v_mov_b32_e32 v5, v0
	v_mov_b32_e32 v6, v0
	v_mov_b32_e32 v7, v0
	v_mov_b32_e32 v8, v0
	v_mov_b32_e32 v9, v0
	v_mov_b32_e32 v10, v0
	v_mov_b32_e32 v11, v0
	v_mov_b32_e32 v12, v0
	v_mov_b32_e32 v13, v0
	v_mov_b32_e32 v14, v0
	v_mov_b32_e32 v15, v0
	v_cmp_lt_i32_e64 s[58:59], 44, v23
	s_nop 1
	s_cmp_lg_u64 s[58:59], 0
	s_cbranch_scc1 .Lagg15_3
	buffer_load_dword v32, v22, s[24:27], 0 offen
	buffer_load_dword v36, v22, s[24:27], 0 offen offset:16
	buffer_load_dword v40, v22, s[24:27], 0 offen offset:32
	buffer_load_dword v44, v22, s[24:27], 0 offen offset:48
	buffer_load_dword v48, v22, s[24:27], 0 offen offset:64
	buffer_load_dword v52, v22, s[24:27], 0 offen offset:80
	buffer_load_dword v56, v22, s[24:27], 0 offen offset:96
	buffer_load_dword v60, v22, s[24:27], 0 offen offset:112
	buffer_load_dword v64, v22, s[24:27], 0 offen offset:128
	buffer_load_dword v65, v22, s[24:27], 0 offen offset:144
	buffer_load_dword v66, v22, s[24:27], 0 offen offset:160
	v_cmp_lt_i32_e64 s[28:29], 0, v23
	v_cmp_lt_i32_e64 s[30:31], 4, v23
	v_cmp_lt_i32_e64 s[32:33], 8, v23
	v_cmp_lt_i32_e64 s[34:35], 12, v23
	v_cmp_lt_i32_e64 s[36:37], 16, v23
	v_cmp_lt_i32_e64 s[38:39], 20, v23
	v_cmp_lt_i32_e64 s[40:41], 24, v23
	v_cmp_lt_i32_e64 s[42:43], 28, v23
	v_cmp_lt_i32_e64 s[44:45], 32, v23
	v_cmp_lt_i32_e64 s[46:47], 36, v23
	v_cmp_lt_i32_e64 s[48:49], 40, v23
	s_waitcnt vmcnt(10)
	v_lshlrev_b32_e32 v71, 4, v32
	v_cndmask_b32_e64 v71, v29, v71, s[28:29]
	buffer_load_dwordx4 v[32:35], v71, s[4:7], 0 offen
	s_waitcnt vmcnt(10)
	v_lshlrev_b32_e32 v71, 4, v36
	v_cndmask_b32_e64 v71, v29, v71, s[30:31]
	buffer_load_dwordx4 v[36:39], v71, s[4:7], 0 offen
	s_waitcnt vmcnt(10)
	v_lshlrev_b32_e32 v71, 4, v40
	v_cndmask_b32_e64 v71, v29, v71, s[32:33]
	buffer_load_dwordx4 v[40:43], v71, s[4:7], 0 offen
	s_waitcnt vmcnt(10)
	v_lshlrev_b32_e32 v71, 4, v44
	v_cndmask_b32_e64 v71, v29, v71, s[34:35]
	buffer_load_dwordx4 v[44:47], v71, s[4:7], 0 offen
	s_waitcnt vmcnt(10)
	v_lshlrev_b32_e32 v71, 4, v48
	v_cndmask_b32_e64 v71, v29, v71, s[36:37]
	buffer_load_dwordx4 v[48:51], v71, s[4:7], 0 offen
	s_waitcnt vmcnt(10)
	v_lshlrev_b32_e32 v71, 4, v52
	v_cndmask_b32_e64 v71, v29, v71, s[38:39]
	buffer_load_dwordx4 v[52:55], v71, s[4:7], 0 offen
	s_waitcnt vmcnt(10)
	v_lshlrev_b32_e32 v71, 4, v56
	v_cndmask_b32_e64 v71, v29, v71, s[40:41]
	buffer_load_dwordx4 v[56:59], v71, s[4:7], 0 offen
	s_waitcnt vmcnt(10)
	v_lshlrev_b32_e32 v71, 4, v60
	v_cndmask_b32_e64 v71, v29, v71, s[42:43]
	buffer_load_dwordx4 v[60:63], v71, s[4:7], 0 offen
	s_waitcnt vmcnt(7)
	v_cvt_pk_f32_fp8_e32 v[16:17], v32
	v_cvt_pk_f32_fp8_sdwa v[24:25], v32 src0_sel:WORD_1
	v_pk_add_f32 v[0:1], v[0:1], v[16:17]
	v_pk_add_f32 v[2:3], v[2:3], v[24:25]
	v_cvt_pk_f32_fp8_e32 v[16:17], v33
	v_cvt_pk_f32_fp8_sdwa v[24:25], v33 src0_sel:WORD_1
	v_pk_add_f32 v[4:5], v[4:5], v[16:17]
	v_pk_add_f32 v[6:7], v[6:7], v[24:25]
	v_cvt_pk_f32_fp8_e32 v[16:17], v34
	v_cvt_pk_f32_fp8_sdwa v[24:25], v34 src0_sel:WORD_1
	v_pk_add_f32 v[8:9], v[8:9], v[16:17]
	v_pk_add_f32 v[10:11], v[10:11], v[24:25]
	v_cvt_pk_f32_fp8_e32 v[16:17], v35
	v_cvt_pk_f32_fp8_sdwa v[24:25], v35 src0_sel:WORD_1
	v_pk_add_f32 v[12:13], v[12:13], v[16:17]
	v_pk_add_f32 v[14:15], v[14:15], v[24:25]
	v_lshlrev_b32_e32 v71, 4, v64
	v_cndmask_b32_e64 v71, v29, v71, s[44:45]
	buffer_load_dwordx4 v[32:35], v71, s[4:7], 0 offen
	s_waitcnt vmcnt(7)
	v_cvt_pk_f32_fp8_e32 v[16:17], v36
	v_cvt_pk_f32_fp8_sdwa v[24:25], v36 src0_sel:WORD_1
	v_pk_add_f32 v[0:1], v[0:1], v[16:17]
	v_pk_add_f32 v[2:3], v[2:3], v[24:25]
	v_cvt_pk_f32_fp8_e32 v[16:17], v37
	v_cvt_pk_f32_fp8_sdwa v[24:25], v37 src0_sel:WORD_1
	v_pk_add_f32 v[4:5], v[4:5], v[16:17]
	v_pk_add_f32 v[6:7], v[6:7], v[24:25]
	v_cvt_pk_f32_fp8_e32 v[16:17], v38
	v_cvt_pk_f32_fp8_sdwa v[24:25], v38 src0_sel:WORD_1
	v_pk_add_f32 v[8:9], v[8:9], v[16:17]
	v_pk_add_f32 v[10:11], v[10:11], v[24:25]
	v_cvt_pk_f32_fp8_e32 v[16:17], v39
	v_cvt_pk_f32_fp8_sdwa v[24:25], v39 src0_sel:WORD_1
	v_pk_add_f32 v[12:13], v[12:13], v[16:17]
	v_pk_add_f32 v[14:15], v[14:15], v[24:25]
	v_lshlrev_b32_e32 v71, 4, v65
	v_cndmask_b32_e64 v71, v29, v71, s[46:47]
	buffer_load_dwordx4 v[36:39], v71, s[4:7], 0 offen
	s_waitcnt vmcnt(7)
	v_cvt_pk_f32_fp8_e32 v[16:17], v40
	v_cvt_pk_f32_fp8_sdwa v[24:25], v40 src0_sel:WORD_1
	v_pk_add_f32 v[0:1], v[0:1], v[16:17]
	v_pk_add_f32 v[2:3], v[2:3], v[24:25]
	v_cvt_pk_f32_fp8_e32 v[16:17], v41
	v_cvt_pk_f32_fp8_sdwa v[24:25], v41 src0_sel:WORD_1
	v_pk_add_f32 v[4:5], v[4:5], v[16:17]
	v_pk_add_f32 v[6:7], v[6:7], v[24:25]
	v_cvt_pk_f32_fp8_e32 v[16:17], v42
	v_cvt_pk_f32_fp8_sdwa v[24:25], v42 src0_sel:WORD_1
	v_pk_add_f32 v[8:9], v[8:9], v[16:17]
	v_pk_add_f32 v[10:11], v[10:11], v[24:25]
	v_cvt_pk_f32_fp8_e32 v[16:17], v43
	v_cvt_pk_f32_fp8_sdwa v[24:25], v43 src0_sel:WORD_1
	v_pk_add_f32 v[12:13], v[12:13], v[16:17]
	v_pk_add_f32 v[14:15], v[14:15], v[24:25]
	v_lshlrev_b32_e32 v71, 4, v66
	v_cndmask_b32_e64 v71, v29, v71, s[48:49]
	buffer_load_dwordx4 v[40:43], v71, s[4:7], 0 offen
	s_waitcnt vmcnt(7)
	v_cvt_pk_f32_fp8_e32 v[16:17], v44
	v_cvt_pk_f32_fp8_sdwa v[24:25], v44 src0_sel:WORD_1
	v_pk_add_f32 v[0:1], v[0:1], v[16:17]
	v_pk_add_f32 v[2:3], v[2:3], v[24:25]
	v_cvt_pk_f32_fp8_e32 v[16:17], v45
	v_cvt_pk_f32_fp8_sdwa v[24:25], v45 src0_sel:WORD_1
	v_pk_add_f32 v[4:5], v[4:5], v[16:17]
	v_pk_add_f32 v[6:7], v[6:7], v[24:25]
	v_cvt_pk_f32_fp8_e32 v[16:17], v46
	v_cvt_pk_f32_fp8_sdwa v[24:25], v46 src0_sel:WORD_1
	v_pk_add_f32 v[8:9], v[8:9], v[16:17]
	v_pk_add_f32 v[10:11], v[10:11], v[24:25]
	v_cvt_pk_f32_fp8_e32 v[16:17], v47
	v_cvt_pk_f32_fp8_sdwa v[24:25], v47 src0_sel:WORD_1
	v_pk_add_f32 v[12:13], v[12:13], v[16:17]
	v_pk_add_f32 v[14:15], v[14:15], v[24:25]
	s_waitcnt vmcnt(6)
	v_cvt_pk_f32_fp8_e32 v[16:17], v48
	v_cvt_pk_f32_fp8_sdwa v[24:25], v48 src0_sel:WORD_1
	v_pk_add_f32 v[0:1], v[0:1], v[16:17]
	v_pk_add_f32 v[2:3], v[2:3], v[24:25]
	v_cvt_pk_f32_fp8_e32 v[16:17], v49
	v_cvt_pk_f32_fp8_sdwa v[24:25], v49 src0_sel:WORD_1
	v_pk_add_f32 v[4:5], v[4:5], v[16:17]
	v_pk_add_f32 v[6:7], v[6:7], v[24:25]
	v_cvt_pk_f32_fp8_e32 v[16:17], v50
	v_cvt_pk_f32_fp8_sdwa v[24:25], v50 src0_sel:WORD_1
	v_pk_add_f32 v[8:9], v[8:9], v[16:17]
	v_pk_add_f32 v[10:11], v[10:11], v[24:25]
	v_cvt_pk_f32_fp8_e32 v[16:17], v51
	v_cvt_pk_f32_fp8_sdwa v[24:25], v51 src0_sel:WORD_1
	v_pk_add_f32 v[12:13], v[12:13], v[16:17]
	v_pk_add_f32 v[14:15], v[14:15], v[24:25]
	s_waitcnt vmcnt(5)
	v_cvt_pk_f32_fp8_e32 v[16:17], v52
	v_cvt_pk_f32_fp8_sdwa v[24:25], v52 src0_sel:WORD_1
	v_pk_add_f32 v[0:1], v[0:1], v[16:17]
	v_pk_add_f32 v[2:3], v[2:3], v[24:25]
	v_cvt_pk_f32_fp8_e32 v[16:17], v53
	v_cvt_pk_f32_fp8_sdwa v[24:25], v53 src0_sel:WORD_1
	v_pk_add_f32 v[4:5], v[4:5], v[16:17]
	v_pk_add_f32 v[6:7], v[6:7], v[24:25]
	v_cvt_pk_f32_fp8_e32 v[16:17], v54
	v_cvt_pk_f32_fp8_sdwa v[24:25], v54 src0_sel:WORD_1
	v_pk_add_f32 v[8:9], v[8:9], v[16:17]
	v_pk_add_f32 v[10:11], v[10:11], v[24:25]
	v_cvt_pk_f32_fp8_e32 v[16:17], v55
	v_cvt_pk_f32_fp8_sdwa v[24:25], v55 src0_sel:WORD_1
	v_pk_add_f32 v[12:13], v[12:13], v[16:17]
	v_pk_add_f32 v[14:15], v[14:15], v[24:25]
	s_waitcnt vmcnt(4)
	v_cvt_pk_f32_fp8_e32 v[16:17], v56
	v_cvt_pk_f32_fp8_sdwa v[24:25], v56 src0_sel:WORD_1
	v_pk_add_f32 v[0:1], v[0:1], v[16:17]
	v_pk_add_f32 v[2:3], v[2:3], v[24:25]
	v_cvt_pk_f32_fp8_e32 v[16:17], v57
	v_cvt_pk_f32_fp8_sdwa v[24:25], v57 src0_sel:WORD_1
	v_pk_add_f32 v[4:5], v[4:5], v[16:17]
	v_pk_add_f32 v[6:7], v[6:7], v[24:25]
	v_cvt_pk_f32_fp8_e32 v[16:17], v58
	v_cvt_pk_f32_fp8_sdwa v[24:25], v58 src0_sel:WORD_1
	v_pk_add_f32 v[8:9], v[8:9], v[16:17]
	v_pk_add_f32 v[10:11], v[10:11], v[24:25]
	v_cvt_pk_f32_fp8_e32 v[16:17], v59
	v_cvt_pk_f32_fp8_sdwa v[24:25], v59 src0_sel:WORD_1
	v_pk_add_f32 v[12:13], v[12:13], v[16:17]
	v_pk_add_f32 v[14:15], v[14:15], v[24:25]
	s_waitcnt vmcnt(3)
	v_cvt_pk_f32_fp8_e32 v[16:17], v60
	v_cvt_pk_f32_fp8_sdwa v[24:25], v60 src0_sel:WORD_1
	v_pk_add_f32 v[0:1], v[0:1], v[16:17]
	v_pk_add_f32 v[2:3], v[2:3], v[24:25]
	v_cvt_pk_f32_fp8_e32 v[16:17], v61
	v_cvt_pk_f32_fp8_sdwa v[24:25], v61 src0_sel:WORD_1
	v_pk_add_f32 v[4:5], v[4:5], v[16:17]
	v_pk_add_f32 v[6:7], v[6:7], v[24:25]
	v_cvt_pk_f32_fp8_e32 v[16:17], v62
	v_cvt_pk_f32_fp8_sdwa v[24:25], v62 src0_sel:WORD_1
	v_pk_add_f32 v[8:9], v[8:9], v[16:17]
	v_pk_add_f32 v[10:11], v[10:11], v[24:25]
	v_cvt_pk_f32_fp8_e32 v[16:17], v63
	v_cvt_pk_f32_fp8_sdwa v[24:25], v63 src0_sel:WORD_1
	v_pk_add_f32 v[12:13], v[12:13], v[16:17]
	v_pk_add_f32 v[14:15], v[14:15], v[24:25]
	s_waitcnt vmcnt(2)
	v_cvt_pk_f32_fp8_e32 v[16:17], v32
	v_cvt_pk_f32_fp8_sdwa v[24:25], v32 src0_sel:WORD_1
	v_pk_add_f32 v[0:1], v[0:1], v[16:17]
	v_pk_add_f32 v[2:3], v[2:3], v[24:25]
	v_cvt_pk_f32_fp8_e32 v[16:17], v33
	v_cvt_pk_f32_fp8_sdwa v[24:25], v33 src0_sel:WORD_1
	v_pk_add_f32 v[4:5], v[4:5], v[16:17]
	v_pk_add_f32 v[6:7], v[6:7], v[24:25]
	v_cvt_pk_f32_fp8_e32 v[16:17], v34
	v_cvt_pk_f32_fp8_sdwa v[24:25], v34 src0_sel:WORD_1
	v_pk_add_f32 v[8:9], v[8:9], v[16:17]
	v_pk_add_f32 v[10:11], v[10:11], v[24:25]
	v_cvt_pk_f32_fp8_e32 v[16:17], v35
	v_cvt_pk_f32_fp8_sdwa v[24:25], v35 src0_sel:WORD_1
	v_pk_add_f32 v[12:13], v[12:13], v[16:17]
	v_pk_add_f32 v[14:15], v[14:15], v[24:25]
	s_waitcnt vmcnt(1)
	v_cvt_pk_f32_fp8_e32 v[16:17], v36
	v_cvt_pk_f32_fp8_sdwa v[24:25], v36 src0_sel:WORD_1
	v_pk_add_f32 v[0:1], v[0:1], v[16:17]
	v_pk_add_f32 v[2:3], v[2:3], v[24:25]
	v_cvt_pk_f32_fp8_e32 v[16:17], v37
	v_cvt_pk_f32_fp8_sdwa v[24:25], v37 src0_sel:WORD_1
	v_pk_add_f32 v[4:5], v[4:5], v[16:17]
	v_pk_add_f32 v[6:7], v[6:7], v[24:25]
	v_cvt_pk_f32_fp8_e32 v[16:17], v38
	v_cvt_pk_f32_fp8_sdwa v[24:25], v38 src0_sel:WORD_1
	v_pk_add_f32 v[8:9], v[8:9], v[16:17]
	v_pk_add_f32 v[10:11], v[10:11], v[24:25]
	v_cvt_pk_f32_fp8_e32 v[16:17], v39
	v_cvt_pk_f32_fp8_sdwa v[24:25], v39 src0_sel:WORD_1
	v_pk_add_f32 v[12:13], v[12:13], v[16:17]
	v_pk_add_f32 v[14:15], v[14:15], v[24:25]
	s_waitcnt vmcnt(0)
	v_cvt_pk_f32_fp8_e32 v[16:17], v40
	v_cvt_pk_f32_fp8_sdwa v[24:25], v40 src0_sel:WORD_1
	v_pk_add_f32 v[0:1], v[0:1], v[16:17]
	v_pk_add_f32 v[2:3], v[2:3], v[24:25]
	v_cvt_pk_f32_fp8_e32 v[16:17], v41
	v_cvt_pk_f32_fp8_sdwa v[24:25], v41 src0_sel:WORD_1
	v_pk_add_f32 v[4:5], v[4:5], v[16:17]
	v_pk_add_f32 v[6:7], v[6:7], v[24:25]
	v_cvt_pk_f32_fp8_e32 v[16:17], v42
	v_cvt_pk_f32_fp8_sdwa v[24:25], v42 src0_sel:WORD_1
	v_pk_add_f32 v[8:9], v[8:9], v[16:17]
	v_pk_add_f32 v[10:11], v[10:11], v[24:25]
	v_cvt_pk_f32_fp8_e32 v[16:17], v43
	v_cvt_pk_f32_fp8_sdwa v[24:25], v43 src0_sel:WORD_1
	v_pk_add_f32 v[12:13], v[12:13], v[16:17]
	v_pk_add_f32 v[14:15], v[14:15], v[24:25]
	s_branch .LBB3_6
.Lagg15_3:
	buffer_load_dword v32, v22, s[24:27], 0 offen
	buffer_load_dword v36, v22, s[24:27], 0 offen offset:16
	buffer_load_dword v40, v22, s[24:27], 0 offen offset:32
	buffer_load_dword v44, v22, s[24:27], 0 offen offset:48
	buffer_load_dword v48, v22, s[24:27], 0 offen offset:64
	buffer_load_dword v52, v22, s[24:27], 0 offen offset:80
	buffer_load_dword v56, v22, s[24:27], 0 offen offset:96
	buffer_load_dword v60, v22, s[24:27], 0 offen offset:112
	buffer_load_dword v64, v22, s[24:27], 0 offen offset:128
	buffer_load_dword v65, v22, s[24:27], 0 offen offset:144
	buffer_load_dword v66, v22, s[24:27], 0 offen offset:160
	buffer_load_dword v67, v22, s[24:27], 0 offen offset:176
	buffer_load_dword v68, v22, s[24:27], 0 offen offset:192
	buffer_load_dword v69, v22, s[24:27], 0 offen offset:208
	buffer_load_dword v70, v22, s[24:27], 0 offen offset:224
	v_cmp_lt_i32_e64 s[28:29], 0, v23
	v_cmp_lt_i32_e64 s[30:31], 4, v23
	v_cmp_lt_i32_e64 s[32:33], 8, v23
	v_cmp_lt_i32_e64 s[34:35], 12, v23
	v_cmp_lt_i32_e64 s[36:37], 16, v23
	v_cmp_lt_i32_e64 s[38:39], 20, v23
	v_cmp_lt_i32_e64 s[40:41], 24, v23
	v_cmp_lt_i32_e64 s[42:43], 28, v23
	v_cmp_lt_i32_e64 s[44:45], 32, v23
	v_cmp_lt_i32_e64 s[46:47], 36, v23
	v_cmp_lt_i32_e64 s[48:49], 40, v23
	v_cmp_lt_i32_e64 s[50:51], 44, v23
	v_cmp_lt_i32_e64 s[52:53], 48, v23
	v_cmp_lt_i32_e64 s[54:55], 52, v23
	v_cmp_lt_i32_e64 s[56:57], 56, v23
	s_waitcnt vmcnt(14)
	v_lshlrev_b32_e32 v71, 4, v32
	v_cndmask_b32_e64 v71, v29, v71, s[28:29]
	buffer_load_dwordx4 v[32:35], v71, s[4:7], 0 offen
	s_waitcnt vmcnt(14)
	v_lshlrev_b32_e32 v71, 4, v36
	v_cndmask_b32_e64 v71, v29, v71, s[30:31]
	buffer_load_dwordx4 v[36:39], v71, s[4:7], 0 offen
	s_waitcnt vmcnt(14)
	v_lshlrev_b32_e32 v71, 4, v40
	v_cndmask_b32_e64 v71, v29, v71, s[32:33]
	buffer_load_dwordx4 v[40:43], v71, s[4:7], 0 offen
	s_waitcnt vmcnt(14)
	v_lshlrev_b32_e32 v71, 4, v44
	v_cndmask_b32_e64 v71, v29, v71, s[34:35]
	buffer_load_dwordx4 v[44:47], v71, s[4:7], 0 offen
	s_waitcnt vmcnt(14)
	v_lshlrev_b32_e32 v71, 4, v48
	v_cndmask_b32_e64 v71, v29, v71, s[36:37]
	buffer_load_dwordx4 v[48:51], v71, s[4:7], 0 offen
	s_waitcnt vmcnt(14)
	v_lshlrev_b32_e32 v71, 4, v52
	v_cndmask_b32_e64 v71, v29, v71, s[38:39]
	buffer_load_dwordx4 v[52:55], v71, s[4:7], 0 offen
	s_waitcnt vmcnt(14)
	v_lshlrev_b32_e32 v71, 4, v56
	v_cndmask_b32_e64 v71, v29, v71, s[40:41]
	buffer_load_dwordx4 v[56:59], v71, s[4:7], 0 offen
	s_waitcnt vmcnt(14)
	v_lshlrev_b32_e32 v71, 4, v60
	v_cndmask_b32_e64 v71, v29, v71, s[42:43]
	buffer_load_dwordx4 v[60:63], v71, s[4:7], 0 offen
	s_waitcnt vmcnt(7)
	v_cvt_pk_f32_fp8_e32 v[16:17], v32
	v_cvt_pk_f32_fp8_sdwa v[24:25], v32 src0_sel:WORD_1
	v_pk_add_f32 v[0:1], v[0:1], v[16:17]
	v_pk_add_f32 v[2:3], v[2:3], v[24:25]
	v_cvt_pk_f32_fp8_e32 v[16:17], v33
	v_cvt_pk_f32_fp8_sdwa v[24:25], v33 src0_sel:WORD_1
	v_pk_add_f32 v[4:5], v[4:5], v[16:17]
	v_pk_add_f32 v[6:7], v[6:7], v[24:25]
	v_cvt_pk_f32_fp8_e32 v[16:17], v34
	v_cvt_pk_f32_fp8_sdwa v[24:25], v34 src0_sel:WORD_1
	v_pk_add_f32 v[8:9], v[8:9], v[16:17]
	v_pk_add_f32 v[10:11], v[10:11], v[24:25]
	v_cvt_pk_f32_fp8_e32 v[16:17], v35
	v_cvt_pk_f32_fp8_sdwa v[24:25], v35 src0_sel:WORD_1
	v_pk_add_f32 v[12:13], v[12:13], v[16:17]
	v_pk_add_f32 v[14:15], v[14:15], v[24:25]
	v_lshlrev_b32_e32 v71, 4, v64
	v_cndmask_b32_e64 v71, v29, v71, s[44:45]
	buffer_load_dwordx4 v[32:35], v71, s[4:7], 0 offen
	s_waitcnt vmcnt(7)
	v_cvt_pk_f32_fp8_e32 v[16:17], v36
	v_cvt_pk_f32_fp8_sdwa v[24:25], v36 src0_sel:WORD_1
	v_pk_add_f32 v[0:1], v[0:1], v[16:17]
	v_pk_add_f32 v[2:3], v[2:3], v[24:25]
	v_cvt_pk_f32_fp8_e32 v[16:17], v37
	v_cvt_pk_f32_fp8_sdwa v[24:25], v37 src0_sel:WORD_1
	v_pk_add_f32 v[4:5], v[4:5], v[16:17]
	v_pk_add_f32 v[6:7], v[6:7], v[24:25]
	v_cvt_pk_f32_fp8_e32 v[16:17], v38
	v_cvt_pk_f32_fp8_sdwa v[24:25], v38 src0_sel:WORD_1
	v_pk_add_f32 v[8:9], v[8:9], v[16:17]
	v_pk_add_f32 v[10:11], v[10:11], v[24:25]
	v_cvt_pk_f32_fp8_e32 v[16:17], v39
	v_cvt_pk_f32_fp8_sdwa v[24:25], v39 src0_sel:WORD_1
	v_pk_add_f32 v[12:13], v[12:13], v[16:17]
	v_pk_add_f32 v[14:15], v[14:15], v[24:25]
	v_lshlrev_b32_e32 v71, 4, v65
	v_cndmask_b32_e64 v71, v29, v71, s[46:47]
	buffer_load_dwordx4 v[36:39], v71, s[4:7], 0 offen
	s_waitcnt vmcnt(7)
	v_cvt_pk_f32_fp8_e32 v[16:17], v40
	v_cvt_pk_f32_fp8_sdwa v[24:25], v40 src0_sel:WORD_1
	v_pk_add_f32 v[0:1], v[0:1], v[16:17]
	v_pk_add_f32 v[2:3], v[2:3], v[24:25]
	v_cvt_pk_f32_fp8_e32 v[16:17], v41
	v_cvt_pk_f32_fp8_sdwa v[24:25], v41 src0_sel:WORD_1
	v_pk_add_f32 v[4:5], v[4:5], v[16:17]
	v_pk_add_f32 v[6:7], v[6:7], v[24:25]
	v_cvt_pk_f32_fp8_e32 v[16:17], v42
	v_cvt_pk_f32_fp8_sdwa v[24:25], v42 src0_sel:WORD_1
	v_pk_add_f32 v[8:9], v[8:9], v[16:17]
	v_pk_add_f32 v[10:11], v[10:11], v[24:25]
	v_cvt_pk_f32_fp8_e32 v[16:17], v43
	v_cvt_pk_f32_fp8_sdwa v[24:25], v43 src0_sel:WORD_1
	v_pk_add_f32 v[12:13], v[12:13], v[16:17]
	v_pk_add_f32 v[14:15], v[14:15], v[24:25]
	v_lshlrev_b32_e32 v71, 4, v66
	v_cndmask_b32_e64 v71, v29, v71, s[48:49]
	buffer_load_dwordx4 v[40:43], v71, s[4:7], 0 offen
	s_waitcnt vmcnt(7)
	v_cvt_pk_f32_fp8_e32 v[16:17], v44
	v_cvt_pk_f32_fp8_sdwa v[24:25], v44 src0_sel:WORD_1
	v_pk_add_f32 v[0:1], v[0:1], v[16:17]
	v_pk_add_f32 v[2:3], v[2:3], v[24:25]
	v_cvt_pk_f32_fp8_e32 v[16:17], v45
	v_cvt_pk_f32_fp8_sdwa v[24:25], v45 src0_sel:WORD_1
	v_pk_add_f32 v[4:5], v[4:5], v[16:17]
	v_pk_add_f32 v[6:7], v[6:7], v[24:25]
	v_cvt_pk_f32_fp8_e32 v[16:17], v46
	v_cvt_pk_f32_fp8_sdwa v[24:25], v46 src0_sel:WORD_1
	v_pk_add_f32 v[8:9], v[8:9], v[16:17]
	v_pk_add_f32 v[10:11], v[10:11], v[24:25]
	v_cvt_pk_f32_fp8_e32 v[16:17], v47
	v_cvt_pk_f32_fp8_sdwa v[24:25], v47 src0_sel:WORD_1
	v_pk_add_f32 v[12:13], v[12:13], v[16:17]
	v_pk_add_f32 v[14:15], v[14:15], v[24:25]
	v_lshlrev_b32_e32 v71, 4, v67
	v_cndmask_b32_e64 v71, v29, v71, s[50:51]
	buffer_load_dwordx4 v[44:47], v71, s[4:7], 0 offen
	s_waitcnt vmcnt(7)
	v_cvt_pk_f32_fp8_e32 v[16:17], v48
	v_cvt_pk_f32_fp8_sdwa v[24:25], v48 src0_sel:WORD_1
	v_pk_add_f32 v[0:1], v[0:1], v[16:17]
	v_pk_add_f32 v[2:3], v[2:3], v[24:25]
	v_cvt_pk_f32_fp8_e32 v[16:17], v49
	v_cvt_pk_f32_fp8_sdwa v[24:25], v49 src0_sel:WORD_1
	v_pk_add_f32 v[4:5], v[4:5], v[16:17]
	v_pk_add_f32 v[6:7], v[6:7], v[24:25]
	v_cvt_pk_f32_fp8_e32 v[16:17], v50
	v_cvt_pk_f32_fp8_sdwa v[24:25], v50 src0_sel:WORD_1
	v_pk_add_f32 v[8:9], v[8:9], v[16:17]
	v_pk_add_f32 v[10:11], v[10:11], v[24:25]
	v_cvt_pk_f32_fp8_e32 v[16:17], v51
	v_cvt_pk_f32_fp8_sdwa v[24:25], v51 src0_sel:WORD_1
	v_pk_add_f32 v[12:13], v[12:13], v[16:17]
	v_pk_add_f32 v[14:15], v[14:15], v[24:25]
	v_lshlrev_b32_e32 v71, 4, v68
	v_cndmask_b32_e64 v71, v29, v71, s[52:53]
	buffer_load_dwordx4 v[48:51], v71, s[4:7], 0 offen
	s_waitcnt vmcnt(7)
	v_cvt_pk_f32_fp8_e32 v[16:17], v52
	v_cvt_pk_f32_fp8_sdwa v[24:25], v52 src0_sel:WORD_1
	v_pk_add_f32 v[0:1], v[0:1], v[16:17]
	v_pk_add_f32 v[2:3], v[2:3], v[24:25]
	v_cvt_pk_f32_fp8_e32 v[16:17], v53
	v_cvt_pk_f32_fp8_sdwa v[24:25], v53 src0_sel:WORD_1
	v_pk_add_f32 v[4:5], v[4:5], v[16:17]
	v_pk_add_f32 v[6:7], v[6:7], v[24:25]
	v_cvt_pk_f32_fp8_e32 v[16:17], v54
	v_cvt_pk_f32_fp8_sdwa v[24:25], v54 src0_sel:WORD_1
	v_pk_add_f32 v[8:9], v[8:9], v[16:17]
	v_pk_add_f32 v[10:11], v[10:11], v[24:25]
	v_cvt_pk_f32_fp8_e32 v[16:17], v55
	v_cvt_pk_f32_fp8_sdwa v[24:25], v55 src0_sel:WORD_1
	v_pk_add_f32 v[12:13], v[12:13], v[16:17]
	v_pk_add_f32 v[14:15], v[14:15], v[24:25]
	v_lshlrev_b32_e32 v71, 4, v69
	v_cndmask_b32_e64 v71, v29, v71, s[54:55]
	buffer_load_dwordx4 v[52:55], v71, s[4:7], 0 offen
	s_waitcnt vmcnt(7)
	v_cvt_pk_f32_fp8_e32 v[16:17], v56
	v_cvt_pk_f32_fp8_sdwa v[24:25], v56 src0_sel:WORD_1
	v_pk_add_f32 v[0:1], v[0:1], v[16:17]
	v_pk_add_f32 v[2:3], v[2:3], v[24:25]
	v_cvt_pk_f32_fp8_e32 v[16:17], v57
	v_cvt_pk_f32_fp8_sdwa v[24:25], v57 src0_sel:WORD_1
	v_pk_add_f32 v[4:5], v[4:5], v[16:17]
	v_pk_add_f32 v[6:7], v[6:7], v[24:25]
	v_cvt_pk_f32_fp8_e32 v[16:17], v58
	v_cvt_pk_f32_fp8_sdwa v[24:25], v58 src0_sel:WORD_1
	v_pk_add_f32 v[8:9], v[8:9], v[16:17]
	v_pk_add_f32 v[10:11], v[10:11], v[24:25]
	v_cvt_pk_f32_fp8_e32 v[16:17], v59
	v_cvt_pk_f32_fp8_sdwa v[24:25], v59 src0_sel:WORD_1
	v_pk_add_f32 v[12:13], v[12:13], v[16:17]
	v_pk_add_f32 v[14:15], v[14:15], v[24:25]
	v_lshlrev_b32_e32 v71, 4, v70
	v_cndmask_b32_e64 v71, v29, v71, s[56:57]
	buffer_load_dwordx4 v[56:59], v71, s[4:7], 0 offen
	s_waitcnt vmcnt(7)
	v_cvt_pk_f32_fp8_e32 v[16:17], v60
	v_cvt_pk_f32_fp8_sdwa v[24:25], v60 src0_sel:WORD_1
	v_pk_add_f32 v[0:1], v[0:1], v[16:17]
	v_pk_add_f32 v[2:3], v[2:3], v[24:25]
	v_cvt_pk_f32_fp8_e32 v[16:17], v61
	v_cvt_pk_f32_fp8_sdwa v[24:25], v61 src0_sel:WORD_1
	v_pk_add_f32 v[4:5], v[4:5], v[16:17]
	v_pk_add_f32 v[6:7], v[6:7], v[24:25]
	v_cvt_pk_f32_fp8_e32 v[16:17], v62
	v_cvt_pk_f32_fp8_sdwa v[24:25], v62 src0_sel:WORD_1
	v_pk_add_f32 v[8:9], v[8:9], v[16:17]
	v_pk_add_f32 v[10:11], v[10:11], v[24:25]
	v_cvt_pk_f32_fp8_e32 v[16:17], v63
	v_cvt_pk_f32_fp8_sdwa v[24:25], v63 src0_sel:WORD_1
	v_pk_add_f32 v[12:13], v[12:13], v[16:17]
	v_pk_add_f32 v[14:15], v[14:15], v[24:25]
	s_waitcnt vmcnt(6)
	v_cvt_pk_f32_fp8_e32 v[16:17], v32
	v_cvt_pk_f32_fp8_sdwa v[24:25], v32 src0_sel:WORD_1
	v_pk_add_f32 v[0:1], v[0:1], v[16:17]
	v_pk_add_f32 v[2:3], v[2:3], v[24:25]
	v_cvt_pk_f32_fp8_e32 v[16:17], v33
	v_cvt_pk_f32_fp8_sdwa v[24:25], v33 src0_sel:WORD_1
	v_pk_add_f32 v[4:5], v[4:5], v[16:17]
	v_pk_add_f32 v[6:7], v[6:7], v[24:25]
	v_cvt_pk_f32_fp8_e32 v[16:17], v34
	v_cvt_pk_f32_fp8_sdwa v[24:25], v34 src0_sel:WORD_1
	v_pk_add_f32 v[8:9], v[8:9], v[16:17]
	v_pk_add_f32 v[10:11], v[10:11], v[24:25]
	v_cvt_pk_f32_fp8_e32 v[16:17], v35
	v_cvt_pk_f32_fp8_sdwa v[24:25], v35 src0_sel:WORD_1
	v_pk_add_f32 v[12:13], v[12:13], v[16:17]
	v_pk_add_f32 v[14:15], v[14:15], v[24:25]
	s_waitcnt vmcnt(5)
	v_cvt_pk_f32_fp8_e32 v[16:17], v36
	v_cvt_pk_f32_fp8_sdwa v[24:25], v36 src0_sel:WORD_1
	v_pk_add_f32 v[0:1], v[0:1], v[16:17]
	v_pk_add_f32 v[2:3], v[2:3], v[24:25]
	v_cvt_pk_f32_fp8_e32 v[16:17], v37
	v_cvt_pk_f32_fp8_sdwa v[24:25], v37 src0_sel:WORD_1
	v_pk_add_f32 v[4:5], v[4:5], v[16:17]
	v_pk_add_f32 v[6:7], v[6:7], v[24:25]
	v_cvt_pk_f32_fp8_e32 v[16:17], v38
	v_cvt_pk_f32_fp8_sdwa v[24:25], v38 src0_sel:WORD_1
	v_pk_add_f32 v[8:9], v[8:9], v[16:17]
	v_pk_add_f32 v[10:11], v[10:11], v[24:25]
	v_cvt_pk_f32_fp8_e32 v[16:17], v39
	v_cvt_pk_f32_fp8_sdwa v[24:25], v39 src0_sel:WORD_1
	v_pk_add_f32 v[12:13], v[12:13], v[16:17]
	v_pk_add_f32 v[14:15], v[14:15], v[24:25]
	s_waitcnt vmcnt(4)
	v_cvt_pk_f32_fp8_e32 v[16:17], v40
	v_cvt_pk_f32_fp8_sdwa v[24:25], v40 src0_sel:WORD_1
	v_pk_add_f32 v[0:1], v[0:1], v[16:17]
	v_pk_add_f32 v[2:3], v[2:3], v[24:25]
	v_cvt_pk_f32_fp8_e32 v[16:17], v41
	v_cvt_pk_f32_fp8_sdwa v[24:25], v41 src0_sel:WORD_1
	v_pk_add_f32 v[4:5], v[4:5], v[16:17]
	v_pk_add_f32 v[6:7], v[6:7], v[24:25]
	v_cvt_pk_f32_fp8_e32 v[16:17], v42
	v_cvt_pk_f32_fp8_sdwa v[24:25], v42 src0_sel:WORD_1
	v_pk_add_f32 v[8:9], v[8:9], v[16:17]
	v_pk_add_f32 v[10:11], v[10:11], v[24:25]
	v_cvt_pk_f32_fp8_e32 v[16:17], v43
	v_cvt_pk_f32_fp8_sdwa v[24:25], v43 src0_sel:WORD_1
	v_pk_add_f32 v[12:13], v[12:13], v[16:17]
	v_pk_add_f32 v[14:15], v[14:15], v[24:25]
	s_waitcnt vmcnt(3)
	v_cvt_pk_f32_fp8_e32 v[16:17], v44
	v_cvt_pk_f32_fp8_sdwa v[24:25], v44 src0_sel:WORD_1
	v_pk_add_f32 v[0:1], v[0:1], v[16:17]
	v_pk_add_f32 v[2:3], v[2:3], v[24:25]
	v_cvt_pk_f32_fp8_e32 v[16:17], v45
	v_cvt_pk_f32_fp8_sdwa v[24:25], v45 src0_sel:WORD_1
	v_pk_add_f32 v[4:5], v[4:5], v[16:17]
	v_pk_add_f32 v[6:7], v[6:7], v[24:25]
	v_cvt_pk_f32_fp8_e32 v[16:17], v46
	v_cvt_pk_f32_fp8_sdwa v[24:25], v46 src0_sel:WORD_1
	v_pk_add_f32 v[8:9], v[8:9], v[16:17]
	v_pk_add_f32 v[10:11], v[10:11], v[24:25]
	v_cvt_pk_f32_fp8_e32 v[16:17], v47
	v_cvt_pk_f32_fp8_sdwa v[24:25], v47 src0_sel:WORD_1
	v_pk_add_f32 v[12:13], v[12:13], v[16:17]
	v_pk_add_f32 v[14:15], v[14:15], v[24:25]
	s_waitcnt vmcnt(2)
	v_cvt_pk_f32_fp8_e32 v[16:17], v48
	v_cvt_pk_f32_fp8_sdwa v[24:25], v48 src0_sel:WORD_1
	v_pk_add_f32 v[0:1], v[0:1], v[16:17]
	v_pk_add_f32 v[2:3], v[2:3], v[24:25]
	v_cvt_pk_f32_fp8_e32 v[16:17], v49
	v_cvt_pk_f32_fp8_sdwa v[24:25], v49 src0_sel:WORD_1
	v_pk_add_f32 v[4:5], v[4:5], v[16:17]
	v_pk_add_f32 v[6:7], v[6:7], v[24:25]
	v_cvt_pk_f32_fp8_e32 v[16:17], v50
	v_cvt_pk_f32_fp8_sdwa v[24:25], v50 src0_sel:WORD_1
	v_pk_add_f32 v[8:9], v[8:9], v[16:17]
	v_pk_add_f32 v[10:11], v[10:11], v[24:25]
	v_cvt_pk_f32_fp8_e32 v[16:17], v51
	v_cvt_pk_f32_fp8_sdwa v[24:25], v51 src0_sel:WORD_1
	v_pk_add_f32 v[12:13], v[12:13], v[16:17]
	v_pk_add_f32 v[14:15], v[14:15], v[24:25]
	s_waitcnt vmcnt(1)
	v_cvt_pk_f32_fp8_e32 v[16:17], v52
	v_cvt_pk_f32_fp8_sdwa v[24:25], v52 src0_sel:WORD_1
	v_pk_add_f32 v[0:1], v[0:1], v[16:17]
	v_pk_add_f32 v[2:3], v[2:3], v[24:25]
	v_cvt_pk_f32_fp8_e32 v[16:17], v53
	v_cvt_pk_f32_fp8_sdwa v[24:25], v53 src0_sel:WORD_1
	v_pk_add_f32 v[4:5], v[4:5], v[16:17]
	v_pk_add_f32 v[6:7], v[6:7], v[24:25]
	v_cvt_pk_f32_fp8_e32 v[16:17], v54
	v_cvt_pk_f32_fp8_sdwa v[24:25], v54 src0_sel:WORD_1
	v_pk_add_f32 v[8:9], v[8:9], v[16:17]
	v_pk_add_f32 v[10:11], v[10:11], v[24:25]
	v_cvt_pk_f32_fp8_e32 v[16:17], v55
	v_cvt_pk_f32_fp8_sdwa v[24:25], v55 src0_sel:WORD_1
	v_pk_add_f32 v[12:13], v[12:13], v[16:17]
	v_pk_add_f32 v[14:15], v[14:15], v[24:25]
	s_waitcnt vmcnt(0)
	v_cvt_pk_f32_fp8_e32 v[16:17], v56
	v_cvt_pk_f32_fp8_sdwa v[24:25], v56 src0_sel:WORD_1
	v_pk_add_f32 v[0:1], v[0:1], v[16:17]
	v_pk_add_f32 v[2:3], v[2:3], v[24:25]
	v_cvt_pk_f32_fp8_e32 v[16:17], v57
	v_cvt_pk_f32_fp8_sdwa v[24:25], v57 src0_sel:WORD_1
	v_pk_add_f32 v[4:5], v[4:5], v[16:17]
	v_pk_add_f32 v[6:7], v[6:7], v[24:25]
	v_cvt_pk_f32_fp8_e32 v[16:17], v58
	v_cvt_pk_f32_fp8_sdwa v[24:25], v58 src0_sel:WORD_1
	v_pk_add_f32 v[8:9], v[8:9], v[16:17]
	v_pk_add_f32 v[10:11], v[10:11], v[24:25]
	v_cvt_pk_f32_fp8_e32 v[16:17], v59
	v_cvt_pk_f32_fp8_sdwa v[24:25], v59 src0_sel:WORD_1
	v_pk_add_f32 v[12:13], v[12:13], v[16:17]
	v_pk_add_f32 v[14:15], v[14:15], v[24:25]
	v_add_u32_e32 v23, 0xffffffc4, v23
	v_add_u32_e32 v22, 0xf0, v22
	v_cmp_lt_i32_e64 s[58:59], 0, v23
	s_nop 1
	s_cmp_lg_u64 s[58:59], 0
	s_cbranch_scc1 .Lagg15_3

.LBB3_8:
	s_mov_b64 exec, -1
	s_nop 4
	v_add_f32_dpp v0, v0, v0 quad_perm:[1,0,3,2] row_mask:0xf bank_mask:0xf
	v_add_f32_dpp v1, v1, v1 quad_perm:[1,0,3,2] row_mask:0xf bank_mask:0xf
	v_add_f32_dpp v2, v2, v2 quad_perm:[1,0,3,2] row_mask:0xf bank_mask:0xf
	v_add_f32_dpp v3, v3, v3 quad_perm:[1,0,3,2] row_mask:0xf bank_mask:0xf
	v_add_f32_dpp v4, v4, v4 quad_perm:[1,0,3,2] row_mask:0xf bank_mask:0xf
	v_add_f32_dpp v5, v5, v5 quad_perm:[1,0,3,2] row_mask:0xf bank_mask:0xf
	v_add_f32_dpp v6, v6, v6 quad_perm:[1,0,3,2] row_mask:0xf bank_mask:0xf
	v_add_f32_dpp v7, v7, v7 quad_perm:[1,0,3,2] row_mask:0xf bank_mask:0xf
	v_add_f32_dpp v8, v8, v8 quad_perm:[1,0,3,2] row_mask:0xf bank_mask:0xf
	v_add_f32_dpp v9, v9, v9 quad_perm:[1,0,3,2] row_mask:0xf bank_mask:0xf
	v_add_f32_dpp v10, v10, v10 quad_perm:[1,0,3,2] row_mask:0xf bank_mask:0xf
	v_add_f32_dpp v11, v11, v11 quad_perm:[1,0,3,2] row_mask:0xf bank_mask:0xf
	v_add_f32_dpp v12, v12, v12 quad_perm:[1,0,3,2] row_mask:0xf bank_mask:0xf
	v_add_f32_dpp v13, v13, v13 quad_perm:[1,0,3,2] row_mask:0xf bank_mask:0xf
	v_add_f32_dpp v14, v14, v14 quad_perm:[1,0,3,2] row_mask:0xf bank_mask:0xf
	v_add_f32_dpp v15, v15, v15 quad_perm:[1,0,3,2] row_mask:0xf bank_mask:0xf
	v_add_f32_dpp v0, v0, v0 quad_perm:[2,3,0,1] row_mask:0xf bank_mask:0xf
	v_add_f32_dpp v1, v1, v1 quad_perm:[2,3,0,1] row_mask:0xf bank_mask:0xf
	v_add_f32_dpp v2, v2, v2 quad_perm:[2,3,0,1] row_mask:0xf bank_mask:0xf
	v_add_f32_dpp v3, v3, v3 quad_perm:[2,3,0,1] row_mask:0xf bank_mask:0xf
	v_add_f32_dpp v4, v4, v4 quad_perm:[2,3,0,1] row_mask:0xf bank_mask:0xf
	v_add_f32_dpp v5, v5, v5 quad_perm:[2,3,0,1] row_mask:0xf bank_mask:0xf
	v_add_f32_dpp v6, v6, v6 quad_perm:[2,3,0,1] row_mask:0xf bank_mask:0xf
	v_add_f32_dpp v7, v7, v7 quad_perm:[2,3,0,1] row_mask:0xf bank_mask:0xf
	v_add_f32_dpp v8, v8, v8 quad_perm:[2,3,0,1] row_mask:0xf bank_mask:0xf
	v_add_f32_dpp v9, v9, v9 quad_perm:[2,3,0,1] row_mask:0xf bank_mask:0xf
	v_add_f32_dpp v10, v10, v10 quad_perm:[2,3,0,1] row_mask:0xf bank_mask:0xf
	v_add_f32_dpp v11, v11, v11 quad_perm:[2,3,0,1] row_mask:0xf bank_mask:0xf
	v_add_f32_dpp v12, v12, v12 quad_perm:[2,3,0,1] row_mask:0xf bank_mask:0xf
	v_add_f32_dpp v13, v13, v13 quad_perm:[2,3,0,1] row_mask:0xf bank_mask:0xf
	v_add_f32_dpp v14, v14, v14 quad_perm:[2,3,0,1] row_mask:0xf bank_mask:0xf
	v_add_f32_dpp v15, v15, v15 quad_perm:[2,3,0,1] row_mask:0xf bank_mask:0xf
	s_and_b64 s[0:1], s[0:1], vcc
	s_and_saveexec_b64 s[2:3], s[0:1]
	s_cbranch_execz .LBB3_10
	s_waitcnt vmcnt(0) lgkmcnt(0)
	v_mul_f32_e32 v16, 0x3d800000, v30
	v_mul_f32_e32 v17, 0x42800000, v30
	v_fma_f32 v0, v16, v0, s60
	v_fma_f32 v1, v16, v1, s61
	v_fma_f32 v2, v16, v2, s62
	v_fma_f32 v3, v16, v3, s63
	v_fma_f32 v4, v16, v4, s64
	v_fma_f32 v5, v16, v5, s65
	v_fma_f32 v6, v16, v6, s66
	v_fma_f32 v7, v16, v7, s67
	v_fma_f32 v8, v16, v8, s68
	v_fma_f32 v9, v16, v9, s69
	v_fma_f32 v10, v16, v10, s70
	v_fma_f32 v11, v16, v11, s71
	v_fma_f32 v12, v16, v12, s72
	v_fma_f32 v13, v16, v13, s73
	v_fma_f32 v14, v16, v14, s74
	v_fma_f32 v15, v16, v15, s75
	v_max_f32_e32 v0, 0, v0
	v_max_f32_e32 v1, 0, v1
	v_max_f32_e32 v2, 0, v2
	v_max_f32_e32 v3, 0, v3
	v_max_f32_e32 v4, 0, v4
	v_max_f32_e32 v5, 0, v5
	v_max_f32_e32 v6, 0, v6
	v_max_f32_e32 v7, 0, v7
	v_max_f32_e32 v8, 0, v8
	v_max_f32_e32 v9, 0, v9
	v_max_f32_e32 v10, 0, v10
	v_max_f32_e32 v11, 0, v11
	v_max_f32_e32 v12, 0, v12
	v_max_f32_e32 v13, 0, v13
	v_max_f32_e32 v14, 0, v14
	v_max_f32_e32 v15, 0, v15
	v_mul_f32_e32 v0, v17, v0
	v_mul_f32_e32 v1, v17, v1
	v_mul_f32_e32 v2, v17, v2
	v_mul_f32_e32 v3, v17, v3
	v_mul_f32_e32 v4, v17, v4
	v_mul_f32_e32 v5, v17, v5
	v_mul_f32_e32 v6, v17, v6
	v_mul_f32_e32 v7, v17, v7
	v_mul_f32_e32 v8, v17, v8
	v_mul_f32_e32 v9, v17, v9
	v_mul_f32_e32 v10, v17, v10
	v_mul_f32_e32 v11, v17, v11
	v_mul_f32_e32 v12, v17, v12
	v_mul_f32_e32 v13, v17, v13
	v_mul_f32_e32 v14, v17, v14
	v_mul_f32_e32 v15, v17, v15
	v_mov_b32_e32 v32, 0
	v_mov_b32_e32 v33, 0
	v_mov_b32_e32 v34, 0
	v_mov_b32_e32 v35, 0
	v_cvt_pk_fp8_f32 v32, v0, v1
	v_cvt_pk_fp8_f32 v33, v4, v5
	v_cvt_pk_fp8_f32 v34, v8, v9
	v_cvt_pk_fp8_f32 v35, v12, v13
	v_cvt_pk_fp8_f32 v32, v2, v3 op_sel:[0,0,1]
	v_cvt_pk_fp8_f32 v33, v6, v7 op_sel:[0,0,1]
	v_cvt_pk_fp8_f32 v34, v10, v11 op_sel:[0,0,1]
	v_cvt_pk_fp8_f32 v35, v14, v15 op_sel:[0,0,1]
	v_lshl_add_u64 v[16:17], v[26:27], 4, s[20:21]
	s_nop 1
	global_store_dwordx4 v[16:17], v[32:35], off

	.amdhsa_kernel _Z5k_aggILi1EEvPKiS1_S1_PKDv4_jPKfS6_PS2_PDF16_
		.amdhsa_group_segment_fixed_size 0
		.amdhsa_private_segment_fixed_size 0
		.amdhsa_kernarg_size 64
		.amdhsa_user_sgpr_count 2
		.amdhsa_user_sgpr_dispatch_ptr 0
		.amdhsa_user_sgpr_queue_ptr 0
		.amdhsa_user_sgpr_kernarg_segment_ptr 1
		.amdhsa_user_sgpr_dispatch_id 0
		.amdhsa_user_sgpr_kernarg_preload_length 0
		.amdhsa_user_sgpr_kernarg_preload_offset 0
		.amdhsa_user_sgpr_private_segment_size 0
		.amdhsa_uses_dynamic_stack 0
		.amdhsa_enable_private_segment 0
		.amdhsa_system_sgpr_workgroup_id_x 1
		.amdhsa_system_sgpr_workgroup_id_y 0
		.amdhsa_system_sgpr_workgroup_id_z 0
		.amdhsa_system_sgpr_workgroup_info 0
		.amdhsa_system_vgpr_workitem_id 0
		.amdhsa_next_free_vgpr 72
		.amdhsa_next_free_sgpr 76
		.amdhsa_accum_offset 72
		.amdhsa_reserve_vcc 1
		.amdhsa_float_round_mode_32 0
		.amdhsa_float_round_mode_16_64 0
		.amdhsa_float_denorm_mode_32 3
		.amdhsa_float_denorm_mode_16_64 3
		.amdhsa_dx10_clamp 1
		.amdhsa_ieee_mode 1
		.amdhsa_fp16_overflow 0
		.amdhsa_tg_split 0
		.amdhsa_exception_fp_ieee_invalid_op 0
		.amdhsa_exception_fp_denorm_src 0
		.amdhsa_exception_fp_ieee_div_zero 0
		.amdhsa_exception_fp_ieee_overflow 0
		.amdhsa_exception_fp_ieee_underflow 0
		.amdhsa_exception_fp_ieee_inexact 0
		.amdhsa_exception_int_div_zero 0
	.end_amdhsa_kernel

_Z5k_aggILi2EEvPKiS1_S1_PKDv4_jPKfS6_PS2_PDF16_:
	s_and_b32 s3, s2, 7
	s_mulk_i32 s3, 0x30e
	s_lshr_b32 s2, s2, 3
	s_add_i32 s3, s3, s2
	v_lshl_or_b32 v1, s3, 6, v0
	v_ashrrev_i32_e32 v1, 2, v1
	s_mov_b32 s2, 0x186a0
	s_load_dwordx8 s[4:11], s[0:1], 0x0
	s_load_dwordx2 s[12:13], s[0:1], 0x20
	v_mov_b32_e32 v2, 0x1869f
	v_cmp_gt_i32_e32 vcc, s2, v1
	v_and_b32_e32 v28, 3, v0
	s_nop 0
	v_cndmask_b32_e32 v26, v2, v1, vcc
	v_ashrrev_i32_e32 v27, 31, v26
	v_lshlrev_b64 v[2:3], 2, v[26:27]
	s_waitcnt lgkmcnt(0)
	v_lshl_add_u64 v[4:5], s[4:5], 0, v[2:3]
	global_load_dword v16, v[4:5], off
	v_lshl_add_u64 v[4:5], s[6:7], 0, v[2:3]
	global_load_dword v1, v[4:5], off
	s_mov_b32 s7, 0x20000
	s_mov_b32 s6, 0x186a00
	s_and_b32 s5, s11, 0xffff
	s_mov_b32 s4, s10
	v_lshlrev_b32_e32 v4, 4, v26
	v_lshl_add_u64 v[2:3], s[12:13], 0, v[2:3]
	buffer_load_dwordx4 v[18:21], v4, s[4:7], 0 offen
	global_load_dword v34, v[2:3], off
	s_waitcnt vmcnt(2)
	v_cndmask_b32_e32 v30, v16, v1, vcc
	v_add_u32_e32 v22, v16, v28
	s_load_dwordx2 s[12:13], s[0:1], 0x38
	s_mov_b32 s24, s8
	s_and_b32 s25, s9, 0xffff
	s_mov_b32 s26, 0x7fffffff
	s_mov_b32 s27, 0x20000
	v_sub_u32_e32 v23, v30, v22
	v_lshlrev_b32_e32 v22, 2, v22
	v_mov_b32_e32 v29, 0x7ffffff0
	v_mov_b32_e32 v0, 0
	v_mov_b32_e32 v1, v0
	v_mov_b32_e32 v2, v0
	v_mov_b32_e32 v3, v0
	v_mov_b32_e32 v4, v0
	v_mov_b32_e32 v5, v0
	v_mov_b32_e32 v6, v0
	v_mov_b32_e32 v7, v0
	v_mov_b32_e32 v8, v0
	v_mov_b32_e32 v9, v0
	v_mov_b32_e32 v10, v0
	v_mov_b32_e32 v11, v0
	v_mov_b32_e32 v12, v0
	v_mov_b32_e32 v13, v0
	v_mov_b32_e32 v14, v0
	v_mov_b32_e32 v15, v0
	v_cmp_lt_i32_e64 s[58:59], 44, v23
	s_nop 1
	s_cmp_lg_u64 s[58:59], 0
	s_cbranch_scc1 .Lagg15_4
	buffer_load_dword v36, v22, s[24:27], 0 offen
	buffer_load_dword v40, v22, s[24:27], 0 offen offset:16
	buffer_load_dword v44, v22, s[24:27], 0 offen offset:32
	buffer_load_dword v48, v22, s[24:27], 0 offen offset:48
	buffer_load_dword v52, v22, s[24:27], 0 offen offset:64
	buffer_load_dword v56, v22, s[24:27], 0 offen offset:80
	buffer_load_dword v60, v22, s[24:27], 0 offen offset:96
	buffer_load_dword v64, v22, s[24:27], 0 offen offset:112
	buffer_load_dword v68, v22, s[24:27], 0 offen offset:128
	buffer_load_dword v69, v22, s[24:27], 0 offen offset:144
	buffer_load_dword v70, v22, s[24:27], 0 offen offset:160
	v_cmp_lt_i32_e64 s[28:29], 0, v23
	v_cmp_lt_i32_e64 s[30:31], 4, v23
	v_cmp_lt_i32_e64 s[32:33], 8, v23
	v_cmp_lt_i32_e64 s[34:35], 12, v23
	v_cmp_lt_i32_e64 s[36:37], 16, v23
	v_cmp_lt_i32_e64 s[38:39], 20, v23
	v_cmp_lt_i32_e64 s[40:41], 24, v23
	v_cmp_lt_i32_e64 s[42:43], 28, v23
	v_cmp_lt_i32_e64 s[44:45], 32, v23
	v_cmp_lt_i32_e64 s[46:47], 36, v23
	v_cmp_lt_i32_e64 s[48:49], 40, v23
	s_waitcnt vmcnt(10)
	v_lshlrev_b32_e32 v35, 4, v36
	v_cndmask_b32_e64 v35, v29, v35, s[28:29]
	buffer_load_dwordx4 v[36:39], v35, s[4:7], 0 offen
	s_waitcnt vmcnt(10)
	v_lshlrev_b32_e32 v35, 4, v40
	v_cndmask_b32_e64 v35, v29, v35, s[30:31]
	buffer_load_dwordx4 v[40:43], v35, s[4:7], 0 offen
	s_waitcnt vmcnt(10)
	v_lshlrev_b32_e32 v35, 4, v44
	v_cndmask_b32_e64 v35, v29, v35, s[32:33]
	buffer_load_dwordx4 v[44:47], v35, s[4:7], 0 offen
	s_waitcnt vmcnt(10)
	v_lshlrev_b32_e32 v35, 4, v48
	v_cndmask_b32_e64 v35, v29, v35, s[34:35]
	buffer_load_dwordx4 v[48:51], v35, s[4:7], 0 offen
	s_waitcnt vmcnt(10)
	v_lshlrev_b32_e32 v35, 4, v52
	v_cndmask_b32_e64 v35, v29, v35, s[36:37]
	buffer_load_dwordx4 v[52:55], v35, s[4:7], 0 offen
	s_waitcnt vmcnt(10)
	v_lshlrev_b32_e32 v35, 4, v56
	v_cndmask_b32_e64 v35, v29, v35, s[38:39]
	buffer_load_dwordx4 v[56:59], v35, s[4:7], 0 offen
	s_waitcnt vmcnt(10)
	v_lshlrev_b32_e32 v35, 4, v60
	v_cndmask_b32_e64 v35, v29, v35, s[40:41]
	buffer_load_dwordx4 v[60:63], v35, s[4:7], 0 offen
	s_waitcnt vmcnt(10)
	v_lshlrev_b32_e32 v35, 4, v64
	v_cndmask_b32_e64 v35, v29, v35, s[42:43]
	buffer_load_dwordx4 v[64:67], v35, s[4:7], 0 offen
	s_waitcnt vmcnt(7)
	v_cvt_pk_f32_fp8_e32 v[16:17], v36
	v_cvt_pk_f32_fp8_sdwa v[24:25], v36 src0_sel:WORD_1
	v_pk_add_f32 v[0:1], v[0:1], v[16:17]
	v_pk_add_f32 v[2:3], v[2:3], v[24:25]
	v_cvt_pk_f32_fp8_e32 v[16:17], v37
	v_cvt_pk_f32_fp8_sdwa v[24:25], v37 src0_sel:WORD_1
	v_pk_add_f32 v[4:5], v[4:5], v[16:17]
	v_pk_add_f32 v[6:7], v[6:7], v[24:25]
	v_cvt_pk_f32_fp8_e32 v[16:17], v38
	v_cvt_pk_f32_fp8_sdwa v[24:25], v38 src0_sel:WORD_1
	v_pk_add_f32 v[8:9], v[8:9], v[16:17]
	v_pk_add_f32 v[10:11], v[10:11], v[24:25]
	v_cvt_pk_f32_fp8_e32 v[16:17], v39
	v_cvt_pk_f32_fp8_sdwa v[24:25], v39 src0_sel:WORD_1
	v_pk_add_f32 v[12:13], v[12:13], v[16:17]
	v_pk_add_f32 v[14:15], v[14:15], v[24:25]
	v_lshlrev_b32_e32 v35, 4, v68
	v_cndmask_b32_e64 v35, v29, v35, s[44:45]
	buffer_load_dwordx4 v[36:39], v35, s[4:7], 0 offen
	s_waitcnt vmcnt(7)
	v_cvt_pk_f32_fp8_e32 v[16:17], v40
	v_cvt_pk_f32_fp8_sdwa v[24:25], v40 src0_sel:WORD_1
	v_pk_add_f32 v[0:1], v[0:1], v[16:17]
	v_pk_add_f32 v[2:3], v[2:3], v[24:25]
	v_cvt_pk_f32_fp8_e32 v[16:17], v41
	v_cvt_pk_f32_fp8_sdwa v[24:25], v41 src0_sel:WORD_1
	v_pk_add_f32 v[4:5], v[4:5], v[16:17]
	v_pk_add_f32 v[6:7], v[6:7], v[24:25]
	v_cvt_pk_f32_fp8_e32 v[16:17], v42
	v_cvt_pk_f32_fp8_sdwa v[24:25], v42 src0_sel:WORD_1
	v_pk_add_f32 v[8:9], v[8:9], v[16:17]
	v_pk_add_f32 v[10:11], v[10:11], v[24:25]
	v_cvt_pk_f32_fp8_e32 v[16:17], v43
	v_cvt_pk_f32_fp8_sdwa v[24:25], v43 src0_sel:WORD_1
	v_pk_add_f32 v[12:13], v[12:13], v[16:17]
	v_pk_add_f32 v[14:15], v[14:15], v[24:25]
	v_lshlrev_b32_e32 v35, 4, v69
	v_cndmask_b32_e64 v35, v29, v35, s[46:47]
	buffer_load_dwordx4 v[40:43], v35, s[4:7], 0 offen
	s_waitcnt vmcnt(7)
	v_cvt_pk_f32_fp8_e32 v[16:17], v44
	v_cvt_pk_f32_fp8_sdwa v[24:25], v44 src0_sel:WORD_1
	v_pk_add_f32 v[0:1], v[0:1], v[16:17]
	v_pk_add_f32 v[2:3], v[2:3], v[24:25]
	v_cvt_pk_f32_fp8_e32 v[16:17], v45
	v_cvt_pk_f32_fp8_sdwa v[24:25], v45 src0_sel:WORD_1
	v_pk_add_f32 v[4:5], v[4:5], v[16:17]
	v_pk_add_f32 v[6:7], v[6:7], v[24:25]
	v_cvt_pk_f32_fp8_e32 v[16:17], v46
	v_cvt_pk_f32_fp8_sdwa v[24:25], v46 src0_sel:WORD_1
	v_pk_add_f32 v[8:9], v[8:9], v[16:17]
	v_pk_add_f32 v[10:11], v[10:11], v[24:25]
	v_cvt_pk_f32_fp8_e32 v[16:17], v47
	v_cvt_pk_f32_fp8_sdwa v[24:25], v47 src0_sel:WORD_1
	v_pk_add_f32 v[12:13], v[12:13], v[16:17]
	v_pk_add_f32 v[14:15], v[14:15], v[24:25]
	v_lshlrev_b32_e32 v35, 4, v70
	v_cndmask_b32_e64 v35, v29, v35, s[48:49]
	buffer_load_dwordx4 v[44:47], v35, s[4:7], 0 offen
	s_waitcnt vmcnt(7)
	v_cvt_pk_f32_fp8_e32 v[16:17], v48
	v_cvt_pk_f32_fp8_sdwa v[24:25], v48 src0_sel:WORD_1
	v_pk_add_f32 v[0:1], v[0:1], v[16:17]
	v_pk_add_f32 v[2:3], v[2:3], v[24:25]
	v_cvt_pk_f32_fp8_e32 v[16:17], v49
	v_cvt_pk_f32_fp8_sdwa v[24:25], v49 src0_sel:WORD_1
	v_pk_add_f32 v[4:5], v[4:5], v[16:17]
	v_pk_add_f32 v[6:7], v[6:7], v[24:25]
	v_cvt_pk_f32_fp8_e32 v[16:17], v50
	v_cvt_pk_f32_fp8_sdwa v[24:25], v50 src0_sel:WORD_1
	v_pk_add_f32 v[8:9], v[8:9], v[16:17]
	v_pk_add_f32 v[10:11], v[10:11], v[24:25]
	v_cvt_pk_f32_fp8_e32 v[16:17], v51
	v_cvt_pk_f32_fp8_sdwa v[24:25], v51 src0_sel:WORD_1
	v_pk_add_f32 v[12:13], v[12:13], v[16:17]
	v_pk_add_f32 v[14:15], v[14:15], v[24:25]
	s_waitcnt vmcnt(6)
	v_cvt_pk_f32_fp8_e32 v[16:17], v52
	v_cvt_pk_f32_fp8_sdwa v[24:25], v52 src0_sel:WORD_1
	v_pk_add_f32 v[0:1], v[0:1], v[16:17]
	v_pk_add_f32 v[2:3], v[2:3], v[24:25]
	v_cvt_pk_f32_fp8_e32 v[16:17], v53
	v_cvt_pk_f32_fp8_sdwa v[24:25], v53 src0_sel:WORD_1
	v_pk_add_f32 v[4:5], v[4:5], v[16:17]
	v_pk_add_f32 v[6:7], v[6:7], v[24:25]
	v_cvt_pk_f32_fp8_e32 v[16:17], v54
	v_cvt_pk_f32_fp8_sdwa v[24:25], v54 src0_sel:WORD_1
	v_pk_add_f32 v[8:9], v[8:9], v[16:17]
	v_pk_add_f32 v[10:11], v[10:11], v[24:25]
	v_cvt_pk_f32_fp8_e32 v[16:17], v55
	v_cvt_pk_f32_fp8_sdwa v[24:25], v55 src0_sel:WORD_1
	v_pk_add_f32 v[12:13], v[12:13], v[16:17]
	v_pk_add_f32 v[14:15], v[14:15], v[24:25]
	s_waitcnt vmcnt(5)
	v_cvt_pk_f32_fp8_e32 v[16:17], v56
	v_cvt_pk_f32_fp8_sdwa v[24:25], v56 src0_sel:WORD_1
	v_pk_add_f32 v[0:1], v[0:1], v[16:17]
	v_pk_add_f32 v[2:3], v[2:3], v[24:25]
	v_cvt_pk_f32_fp8_e32 v[16:17], v57
	v_cvt_pk_f32_fp8_sdwa v[24:25], v57 src0_sel:WORD_1
	v_pk_add_f32 v[4:5], v[4:5], v[16:17]
	v_pk_add_f32 v[6:7], v[6:7], v[24:25]
	v_cvt_pk_f32_fp8_e32 v[16:17], v58
	v_cvt_pk_f32_fp8_sdwa v[24:25], v58 src0_sel:WORD_1
	v_pk_add_f32 v[8:9], v[8:9], v[16:17]
	v_pk_add_f32 v[10:11], v[10:11], v[24:25]
	v_cvt_pk_f32_fp8_e32 v[16:17], v59
	v_cvt_pk_f32_fp8_sdwa v[24:25], v59 src0_sel:WORD_1
	v_pk_add_f32 v[12:13], v[12:13], v[16:17]
	v_pk_add_f32 v[14:15], v[14:15], v[24:25]
	s_waitcnt vmcnt(4)
	v_cvt_pk_f32_fp8_e32 v[16:17], v60
	v_cvt_pk_f32_fp8_sdwa v[24:25], v60 src0_sel:WORD_1
	v_pk_add_f32 v[0:1], v[0:1], v[16:17]
	v_pk_add_f32 v[2:3], v[2:3], v[24:25]
	v_cvt_pk_f32_fp8_e32 v[16:17], v61
	v_cvt_pk_f32_fp8_sdwa v[24:25], v61 src0_sel:WORD_1
	v_pk_add_f32 v[4:5], v[4:5], v[16:17]
	v_pk_add_f32 v[6:7], v[6:7], v[24:25]
	v_cvt_pk_f32_fp8_e32 v[16:17], v62
	v_cvt_pk_f32_fp8_sdwa v[24:25], v62 src0_sel:WORD_1
	v_pk_add_f32 v[8:9], v[8:9], v[16:17]
	v_pk_add_f32 v[10:11], v[10:11], v[24:25]
	v_cvt_pk_f32_fp8_e32 v[16:17], v63
	v_cvt_pk_f32_fp8_sdwa v[24:25], v63 src0_sel:WORD_1
	v_pk_add_f32 v[12:13], v[12:13], v[16:17]
	v_pk_add_f32 v[14:15], v[14:15], v[24:25]
	s_waitcnt vmcnt(3)
	v_cvt_pk_f32_fp8_e32 v[16:17], v64
	v_cvt_pk_f32_fp8_sdwa v[24:25], v64 src0_sel:WORD_1
	v_pk_add_f32 v[0:1], v[0:1], v[16:17]
	v_pk_add_f32 v[2:3], v[2:3], v[24:25]
	v_cvt_pk_f32_fp8_e32 v[16:17], v65
	v_cvt_pk_f32_fp8_sdwa v[24:25], v65 src0_sel:WORD_1
	v_pk_add_f32 v[4:5], v[4:5], v[16:17]
	v_pk_add_f32 v[6:7], v[6:7], v[24:25]
	v_cvt_pk_f32_fp8_e32 v[16:17], v66
	v_cvt_pk_f32_fp8_sdwa v[24:25], v66 src0_sel:WORD_1
	v_pk_add_f32 v[8:9], v[8:9], v[16:17]
	v_pk_add_f32 v[10:11], v[10:11], v[24:25]
	v_cvt_pk_f32_fp8_e32 v[16:17], v67
	v_cvt_pk_f32_fp8_sdwa v[24:25], v67 src0_sel:WORD_1
	v_pk_add_f32 v[12:13], v[12:13], v[16:17]
	v_pk_add_f32 v[14:15], v[14:15], v[24:25]
	s_waitcnt vmcnt(2)
	v_cvt_pk_f32_fp8_e32 v[16:17], v36
	v_cvt_pk_f32_fp8_sdwa v[24:25], v36 src0_sel:WORD_1
	v_pk_add_f32 v[0:1], v[0:1], v[16:17]
	v_pk_add_f32 v[2:3], v[2:3], v[24:25]
	v_cvt_pk_f32_fp8_e32 v[16:17], v37
	v_cvt_pk_f32_fp8_sdwa v[24:25], v37 src0_sel:WORD_1
	v_pk_add_f32 v[4:5], v[4:5], v[16:17]
	v_pk_add_f32 v[6:7], v[6:7], v[24:25]
	v_cvt_pk_f32_fp8_e32 v[16:17], v38
	v_cvt_pk_f32_fp8_sdwa v[24:25], v38 src0_sel:WORD_1
	v_pk_add_f32 v[8:9], v[8:9], v[16:17]
	v_pk_add_f32 v[10:11], v[10:11], v[24:25]
	v_cvt_pk_f32_fp8_e32 v[16:17], v39
	v_cvt_pk_f32_fp8_sdwa v[24:25], v39 src0_sel:WORD_1
	v_pk_add_f32 v[12:13], v[12:13], v[16:17]
	v_pk_add_f32 v[14:15], v[14:15], v[24:25]
	s_waitcnt vmcnt(1)
	v_cvt_pk_f32_fp8_e32 v[16:17], v40
	v_cvt_pk_f32_fp8_sdwa v[24:25], v40 src0_sel:WORD_1
	v_pk_add_f32 v[0:1], v[0:1], v[16:17]
	v_pk_add_f32 v[2:3], v[2:3], v[24:25]
	v_cvt_pk_f32_fp8_e32 v[16:17], v41
	v_cvt_pk_f32_fp8_sdwa v[24:25], v41 src0_sel:WORD_1
	v_pk_add_f32 v[4:5], v[4:5], v[16:17]
	v_pk_add_f32 v[6:7], v[6:7], v[24:25]
	v_cvt_pk_f32_fp8_e32 v[16:17], v42
	v_cvt_pk_f32_fp8_sdwa v[24:25], v42 src0_sel:WORD_1
	v_pk_add_f32 v[8:9], v[8:9], v[16:17]
	v_pk_add_f32 v[10:11], v[10:11], v[24:25]
	v_cvt_pk_f32_fp8_e32 v[16:17], v43
	v_cvt_pk_f32_fp8_sdwa v[24:25], v43 src0_sel:WORD_1
	v_pk_add_f32 v[12:13], v[12:13], v[16:17]
	v_pk_add_f32 v[14:15], v[14:15], v[24:25]
	s_waitcnt vmcnt(0)
	v_cvt_pk_f32_fp8_e32 v[16:17], v44
	v_cvt_pk_f32_fp8_sdwa v[24:25], v44 src0_sel:WORD_1
	v_pk_add_f32 v[0:1], v[0:1], v[16:17]
	v_pk_add_f32 v[2:3], v[2:3], v[24:25]
	v_cvt_pk_f32_fp8_e32 v[16:17], v45
	v_cvt_pk_f32_fp8_sdwa v[24:25], v45 src0_sel:WORD_1
	v_pk_add_f32 v[4:5], v[4:5], v[16:17]
	v_pk_add_f32 v[6:7], v[6:7], v[24:25]
	v_cvt_pk_f32_fp8_e32 v[16:17], v46
	v_cvt_pk_f32_fp8_sdwa v[24:25], v46 src0_sel:WORD_1
	v_pk_add_f32 v[8:9], v[8:9], v[16:17]
	v_pk_add_f32 v[10:11], v[10:11], v[24:25]
	v_cvt_pk_f32_fp8_e32 v[16:17], v47
	v_cvt_pk_f32_fp8_sdwa v[24:25], v47 src0_sel:WORD_1
	v_pk_add_f32 v[12:13], v[12:13], v[16:17]
	v_pk_add_f32 v[14:15], v[14:15], v[24:25]
	s_branch .LBB4_6
.Lagg15_4:
	buffer_load_dword v36, v22, s[24:27], 0 offen
	buffer_load_dword v40, v22, s[24:27], 0 offen offset:16
	buffer_load_dword v44, v22, s[24:27], 0 offen offset:32
	buffer_load_dword v48, v22, s[24:27], 0 offen offset:48
	buffer_load_dword v52, v22, s[24:27], 0 offen offset:64
	buffer_load_dword v56, v22, s[24:27], 0 offen offset:80
	buffer_load_dword v60, v22, s[24:27], 0 offen offset:96
	buffer_load_dword v64, v22, s[24:27], 0 offen offset:112
	buffer_load_dword v68, v22, s[24:27], 0 offen offset:128
	buffer_load_dword v69, v22, s[24:27], 0 offen offset:144
	buffer_load_dword v70, v22, s[24:27], 0 offen offset:160
	buffer_load_dword v71, v22, s[24:27], 0 offen offset:176
	buffer_load_dword v31, v22, s[24:27], 0 offen offset:192
	buffer_load_dword v32, v22, s[24:27], 0 offen offset:208
	buffer_load_dword v33, v22, s[24:27], 0 offen offset:224
	v_cmp_lt_i32_e64 s[28:29], 0, v23
	v_cmp_lt_i32_e64 s[30:31], 4, v23
	v_cmp_lt_i32_e64 s[32:33], 8, v23
	v_cmp_lt_i32_e64 s[34:35], 12, v23
	v_cmp_lt_i32_e64 s[36:37], 16, v23
	v_cmp_lt_i32_e64 s[38:39], 20, v23
	v_cmp_lt_i32_e64 s[40:41], 24, v23
	v_cmp_lt_i32_e64 s[42:43], 28, v23
	v_cmp_lt_i32_e64 s[44:45], 32, v23
	v_cmp_lt_i32_e64 s[46:47], 36, v23
	v_cmp_lt_i32_e64 s[48:49], 40, v23
	v_cmp_lt_i32_e64 s[50:51], 44, v23
	v_cmp_lt_i32_e64 s[52:53], 48, v23
	v_cmp_lt_i32_e64 s[54:55], 52, v23
	v_cmp_lt_i32_e64 s[56:57], 56, v23
	s_waitcnt vmcnt(14)
	v_lshlrev_b32_e32 v35, 4, v36
	v_cndmask_b32_e64 v35, v29, v35, s[28:29]
	buffer_load_dwordx4 v[36:39], v35, s[4:7], 0 offen
	s_waitcnt vmcnt(14)
	v_lshlrev_b32_e32 v35, 4, v40
	v_cndmask_b32_e64 v35, v29, v35, s[30:31]
	buffer_load_dwordx4 v[40:43], v35, s[4:7], 0 offen
	s_waitcnt vmcnt(14)
	v_lshlrev_b32_e32 v35, 4, v44
	v_cndmask_b32_e64 v35, v29, v35, s[32:33]
	buffer_load_dwordx4 v[44:47], v35, s[4:7], 0 offen
	s_waitcnt vmcnt(14)
	v_lshlrev_b32_e32 v35, 4, v48
	v_cndmask_b32_e64 v35, v29, v35, s[34:35]
	buffer_load_dwordx4 v[48:51], v35, s[4:7], 0 offen
	s_waitcnt vmcnt(14)
	v_lshlrev_b32_e32 v35, 4, v52
	v_cndmask_b32_e64 v35, v29, v35, s[36:37]
	buffer_load_dwordx4 v[52:55], v35, s[4:7], 0 offen
	s_waitcnt vmcnt(14)
	v_lshlrev_b32_e32 v35, 4, v56
	v_cndmask_b32_e64 v35, v29, v35, s[38:39]
	buffer_load_dwordx4 v[56:59], v35, s[4:7], 0 offen
	s_waitcnt vmcnt(14)
	v_lshlrev_b32_e32 v35, 4, v60
	v_cndmask_b32_e64 v35, v29, v35, s[40:41]
	buffer_load_dwordx4 v[60:63], v35, s[4:7], 0 offen
	s_waitcnt vmcnt(14)
	v_lshlrev_b32_e32 v35, 4, v64
	v_cndmask_b32_e64 v35, v29, v35, s[42:43]
	buffer_load_dwordx4 v[64:67], v35, s[4:7], 0 offen
	s_waitcnt vmcnt(7)
	v_cvt_pk_f32_fp8_e32 v[16:17], v36
	v_cvt_pk_f32_fp8_sdwa v[24:25], v36 src0_sel:WORD_1
	v_pk_add_f32 v[0:1], v[0:1], v[16:17]
	v_pk_add_f32 v[2:3], v[2:3], v[24:25]
	v_cvt_pk_f32_fp8_e32 v[16:17], v37
	v_cvt_pk_f32_fp8_sdwa v[24:25], v37 src0_sel:WORD_1
	v_pk_add_f32 v[4:5], v[4:5], v[16:17]
	v_pk_add_f32 v[6:7], v[6:7], v[24:25]
	v_cvt_pk_f32_fp8_e32 v[16:17], v38
	v_cvt_pk_f32_fp8_sdwa v[24:25], v38 src0_sel:WORD_1
	v_pk_add_f32 v[8:9], v[8:9], v[16:17]
	v_pk_add_f32 v[10:11], v[10:11], v[24:25]
	v_cvt_pk_f32_fp8_e32 v[16:17], v39
	v_cvt_pk_f32_fp8_sdwa v[24:25], v39 src0_sel:WORD_1
	v_pk_add_f32 v[12:13], v[12:13], v[16:17]
	v_pk_add_f32 v[14:15], v[14:15], v[24:25]
	v_lshlrev_b32_e32 v35, 4, v68
	v_cndmask_b32_e64 v35, v29, v35, s[44:45]
	buffer_load_dwordx4 v[36:39], v35, s[4:7], 0 offen
	s_waitcnt vmcnt(7)
	v_cvt_pk_f32_fp8_e32 v[16:17], v40
	v_cvt_pk_f32_fp8_sdwa v[24:25], v40 src0_sel:WORD_1
	v_pk_add_f32 v[0:1], v[0:1], v[16:17]
	v_pk_add_f32 v[2:3], v[2:3], v[24:25]
	v_cvt_pk_f32_fp8_e32 v[16:17], v41
	v_cvt_pk_f32_fp8_sdwa v[24:25], v41 src0_sel:WORD_1
	v_pk_add_f32 v[4:5], v[4:5], v[16:17]
	v_pk_add_f32 v[6:7], v[6:7], v[24:25]
	v_cvt_pk_f32_fp8_e32 v[16:17], v42
	v_cvt_pk_f32_fp8_sdwa v[24:25], v42 src0_sel:WORD_1
	v_pk_add_f32 v[8:9], v[8:9], v[16:17]
	v_pk_add_f32 v[10:11], v[10:11], v[24:25]
	v_cvt_pk_f32_fp8_e32 v[16:17], v43
	v_cvt_pk_f32_fp8_sdwa v[24:25], v43 src0_sel:WORD_1
	v_pk_add_f32 v[12:13], v[12:13], v[16:17]
	v_pk_add_f32 v[14:15], v[14:15], v[24:25]
	v_lshlrev_b32_e32 v35, 4, v69
	v_cndmask_b32_e64 v35, v29, v35, s[46:47]
	buffer_load_dwordx4 v[40:43], v35, s[4:7], 0 offen
	s_waitcnt vmcnt(7)
	v_cvt_pk_f32_fp8_e32 v[16:17], v44
	v_cvt_pk_f32_fp8_sdwa v[24:25], v44 src0_sel:WORD_1
	v_pk_add_f32 v[0:1], v[0:1], v[16:17]
	v_pk_add_f32 v[2:3], v[2:3], v[24:25]
	v_cvt_pk_f32_fp8_e32 v[16:17], v45
	v_cvt_pk_f32_fp8_sdwa v[24:25], v45 src0_sel:WORD_1
	v_pk_add_f32 v[4:5], v[4:5], v[16:17]
	v_pk_add_f32 v[6:7], v[6:7], v[24:25]
	v_cvt_pk_f32_fp8_e32 v[16:17], v46
	v_cvt_pk_f32_fp8_sdwa v[24:25], v46 src0_sel:WORD_1
	v_pk_add_f32 v[8:9], v[8:9], v[16:17]
	v_pk_add_f32 v[10:11], v[10:11], v[24:25]
	v_cvt_pk_f32_fp8_e32 v[16:17], v47
	v_cvt_pk_f32_fp8_sdwa v[24:25], v47 src0_sel:WORD_1
	v_pk_add_f32 v[12:13], v[12:13], v[16:17]
	v_pk_add_f32 v[14:15], v[14:15], v[24:25]
	v_lshlrev_b32_e32 v35, 4, v70
	v_cndmask_b32_e64 v35, v29, v35, s[48:49]
	buffer_load_dwordx4 v[44:47], v35, s[4:7], 0 offen
	s_waitcnt vmcnt(7)
	v_cvt_pk_f32_fp8_e32 v[16:17], v48
	v_cvt_pk_f32_fp8_sdwa v[24:25], v48 src0_sel:WORD_1
	v_pk_add_f32 v[0:1], v[0:1], v[16:17]
	v_pk_add_f32 v[2:3], v[2:3], v[24:25]
	v_cvt_pk_f32_fp8_e32 v[16:17], v49
	v_cvt_pk_f32_fp8_sdwa v[24:25], v49 src0_sel:WORD_1
	v_pk_add_f32 v[4:5], v[4:5], v[16:17]
	v_pk_add_f32 v[6:7], v[6:7], v[24:25]
	v_cvt_pk_f32_fp8_e32 v[16:17], v50
	v_cvt_pk_f32_fp8_sdwa v[24:25], v50 src0_sel:WORD_1
	v_pk_add_f32 v[8:9], v[8:9], v[16:17]
	v_pk_add_f32 v[10:11], v[10:11], v[24:25]
	v_cvt_pk_f32_fp8_e32 v[16:17], v51
	v_cvt_pk_f32_fp8_sdwa v[24:25], v51 src0_sel:WORD_1
	v_pk_add_f32 v[12:13], v[12:13], v[16:17]
	v_pk_add_f32 v[14:15], v[14:15], v[24:25]
	v_lshlrev_b32_e32 v35, 4, v71
	v_cndmask_b32_e64 v35, v29, v35, s[50:51]
	buffer_load_dwordx4 v[48:51], v35, s[4:7], 0 offen
	s_waitcnt vmcnt(7)
	v_cvt_pk_f32_fp8_e32 v[16:17], v52
	v_cvt_pk_f32_fp8_sdwa v[24:25], v52 src0_sel:WORD_1
	v_pk_add_f32 v[0:1], v[0:1], v[16:17]
	v_pk_add_f32 v[2:3], v[2:3], v[24:25]
	v_cvt_pk_f32_fp8_e32 v[16:17], v53
	v_cvt_pk_f32_fp8_sdwa v[24:25], v53 src0_sel:WORD_1
	v_pk_add_f32 v[4:5], v[4:5], v[16:17]
	v_pk_add_f32 v[6:7], v[6:7], v[24:25]
	v_cvt_pk_f32_fp8_e32 v[16:17], v54
	v_cvt_pk_f32_fp8_sdwa v[24:25], v54 src0_sel:WORD_1
	v_pk_add_f32 v[8:9], v[8:9], v[16:17]
	v_pk_add_f32 v[10:11], v[10:11], v[24:25]
	v_cvt_pk_f32_fp8_e32 v[16:17], v55
	v_cvt_pk_f32_fp8_sdwa v[24:25], v55 src0_sel:WORD_1
	v_pk_add_f32 v[12:13], v[12:13], v[16:17]
	v_pk_add_f32 v[14:15], v[14:15], v[24:25]
	v_lshlrev_b32_e32 v35, 4, v31
	v_cndmask_b32_e64 v35, v29, v35, s[52:53]
	buffer_load_dwordx4 v[52:55], v35, s[4:7], 0 offen
	s_waitcnt vmcnt(7)
	v_cvt_pk_f32_fp8_e32 v[16:17], v56
	v_cvt_pk_f32_fp8_sdwa v[24:25], v56 src0_sel:WORD_1
	v_pk_add_f32 v[0:1], v[0:1], v[16:17]
	v_pk_add_f32 v[2:3], v[2:3], v[24:25]
	v_cvt_pk_f32_fp8_e32 v[16:17], v57
	v_cvt_pk_f32_fp8_sdwa v[24:25], v57 src0_sel:WORD_1
	v_pk_add_f32 v[4:5], v[4:5], v[16:17]
	v_pk_add_f32 v[6:7], v[6:7], v[24:25]
	v_cvt_pk_f32_fp8_e32 v[16:17], v58
	v_cvt_pk_f32_fp8_sdwa v[24:25], v58 src0_sel:WORD_1
	v_pk_add_f32 v[8:9], v[8:9], v[16:17]
	v_pk_add_f32 v[10:11], v[10:11], v[24:25]
	v_cvt_pk_f32_fp8_e32 v[16:17], v59
	v_cvt_pk_f32_fp8_sdwa v[24:25], v59 src0_sel:WORD_1
	v_pk_add_f32 v[12:13], v[12:13], v[16:17]
	v_pk_add_f32 v[14:15], v[14:15], v[24:25]
	v_lshlrev_b32_e32 v35, 4, v32
	v_cndmask_b32_e64 v35, v29, v35, s[54:55]
	buffer_load_dwordx4 v[56:59], v35, s[4:7], 0 offen
	s_waitcnt vmcnt(7)
	v_cvt_pk_f32_fp8_e32 v[16:17], v60
	v_cvt_pk_f32_fp8_sdwa v[24:25], v60 src0_sel:WORD_1
	v_pk_add_f32 v[0:1], v[0:1], v[16:17]
	v_pk_add_f32 v[2:3], v[2:3], v[24:25]
	v_cvt_pk_f32_fp8_e32 v[16:17], v61
	v_cvt_pk_f32_fp8_sdwa v[24:25], v61 src0_sel:WORD_1
	v_pk_add_f32 v[4:5], v[4:5], v[16:17]
	v_pk_add_f32 v[6:7], v[6:7], v[24:25]
	v_cvt_pk_f32_fp8_e32 v[16:17], v62
	v_cvt_pk_f32_fp8_sdwa v[24:25], v62 src0_sel:WORD_1
	v_pk_add_f32 v[8:9], v[8:9], v[16:17]
	v_pk_add_f32 v[10:11], v[10:11], v[24:25]
	v_cvt_pk_f32_fp8_e32 v[16:17], v63
	v_cvt_pk_f32_fp8_sdwa v[24:25], v63 src0_sel:WORD_1
	v_pk_add_f32 v[12:13], v[12:13], v[16:17]
	v_pk_add_f32 v[14:15], v[14:15], v[24:25]
	v_lshlrev_b32_e32 v35, 4, v33
	v_cndmask_b32_e64 v35, v29, v35, s[56:57]
	buffer_load_dwordx4 v[60:63], v35, s[4:7], 0 offen
	s_waitcnt vmcnt(7)
	v_cvt_pk_f32_fp8_e32 v[16:17], v64
	v_cvt_pk_f32_fp8_sdwa v[24:25], v64 src0_sel:WORD_1
	v_pk_add_f32 v[0:1], v[0:1], v[16:17]
	v_pk_add_f32 v[2:3], v[2:3], v[24:25]
	v_cvt_pk_f32_fp8_e32 v[16:17], v65
	v_cvt_pk_f32_fp8_sdwa v[24:25], v65 src0_sel:WORD_1
	v_pk_add_f32 v[4:5], v[4:5], v[16:17]
	v_pk_add_f32 v[6:7], v[6:7], v[24:25]
	v_cvt_pk_f32_fp8_e32 v[16:17], v66
	v_cvt_pk_f32_fp8_sdwa v[24:25], v66 src0_sel:WORD_1
	v_pk_add_f32 v[8:9], v[8:9], v[16:17]
	v_pk_add_f32 v[10:11], v[10:11], v[24:25]
	v_cvt_pk_f32_fp8_e32 v[16:17], v67
	v_cvt_pk_f32_fp8_sdwa v[24:25], v67 src0_sel:WORD_1
	v_pk_add_f32 v[12:13], v[12:13], v[16:17]
	v_pk_add_f32 v[14:15], v[14:15], v[24:25]
	s_waitcnt vmcnt(6)
	v_cvt_pk_f32_fp8_e32 v[16:17], v36
	v_cvt_pk_f32_fp8_sdwa v[24:25], v36 src0_sel:WORD_1
	v_pk_add_f32 v[0:1], v[0:1], v[16:17]
	v_pk_add_f32 v[2:3], v[2:3], v[24:25]
	v_cvt_pk_f32_fp8_e32 v[16:17], v37
	v_cvt_pk_f32_fp8_sdwa v[24:25], v37 src0_sel:WORD_1
	v_pk_add_f32 v[4:5], v[4:5], v[16:17]
	v_pk_add_f32 v[6:7], v[6:7], v[24:25]
	v_cvt_pk_f32_fp8_e32 v[16:17], v38
	v_cvt_pk_f32_fp8_sdwa v[24:25], v38 src0_sel:WORD_1
	v_pk_add_f32 v[8:9], v[8:9], v[16:17]
	v_pk_add_f32 v[10:11], v[10:11], v[24:25]
	v_cvt_pk_f32_fp8_e32 v[16:17], v39
	v_cvt_pk_f32_fp8_sdwa v[24:25], v39 src0_sel:WORD_1
	v_pk_add_f32 v[12:13], v[12:13], v[16:17]
	v_pk_add_f32 v[14:15], v[14:15], v[24:25]
	s_waitcnt vmcnt(5)
	v_cvt_pk_f32_fp8_e32 v[16:17], v40
	v_cvt_pk_f32_fp8_sdwa v[24:25], v40 src0_sel:WORD_1
	v_pk_add_f32 v[0:1], v[0:1], v[16:17]
	v_pk_add_f32 v[2:3], v[2:3], v[24:25]
	v_cvt_pk_f32_fp8_e32 v[16:17], v41
	v_cvt_pk_f32_fp8_sdwa v[24:25], v41 src0_sel:WORD_1
	v_pk_add_f32 v[4:5], v[4:5], v[16:17]
	v_pk_add_f32 v[6:7], v[6:7], v[24:25]
	v_cvt_pk_f32_fp8_e32 v[16:17], v42
	v_cvt_pk_f32_fp8_sdwa v[24:25], v42 src0_sel:WORD_1
	v_pk_add_f32 v[8:9], v[8:9], v[16:17]
	v_pk_add_f32 v[10:11], v[10:11], v[24:25]
	v_cvt_pk_f32_fp8_e32 v[16:17], v43
	v_cvt_pk_f32_fp8_sdwa v[24:25], v43 src0_sel:WORD_1
	v_pk_add_f32 v[12:13], v[12:13], v[16:17]
	v_pk_add_f32 v[14:15], v[14:15], v[24:25]
	s_waitcnt vmcnt(4)
	v_cvt_pk_f32_fp8_e32 v[16:17], v44
	v_cvt_pk_f32_fp8_sdwa v[24:25], v44 src0_sel:WORD_1
	v_pk_add_f32 v[0:1], v[0:1], v[16:17]
	v_pk_add_f32 v[2:3], v[2:3], v[24:25]
	v_cvt_pk_f32_fp8_e32 v[16:17], v45
	v_cvt_pk_f32_fp8_sdwa v[24:25], v45 src0_sel:WORD_1
	v_pk_add_f32 v[4:5], v[4:5], v[16:17]
	v_pk_add_f32 v[6:7], v[6:7], v[24:25]
	v_cvt_pk_f32_fp8_e32 v[16:17], v46
	v_cvt_pk_f32_fp8_sdwa v[24:25], v46 src0_sel:WORD_1
	v_pk_add_f32 v[8:9], v[8:9], v[16:17]
	v_pk_add_f32 v[10:11], v[10:11], v[24:25]
	v_cvt_pk_f32_fp8_e32 v[16:17], v47
	v_cvt_pk_f32_fp8_sdwa v[24:25], v47 src0_sel:WORD_1
	v_pk_add_f32 v[12:13], v[12:13], v[16:17]
	v_pk_add_f32 v[14:15], v[14:15], v[24:25]
	s_waitcnt vmcnt(3)
	v_cvt_pk_f32_fp8_e32 v[16:17], v48
	v_cvt_pk_f32_fp8_sdwa v[24:25], v48 src0_sel:WORD_1
	v_pk_add_f32 v[0:1], v[0:1], v[16:17]
	v_pk_add_f32 v[2:3], v[2:3], v[24:25]
	v_cvt_pk_f32_fp8_e32 v[16:17], v49
	v_cvt_pk_f32_fp8_sdwa v[24:25], v49 src0_sel:WORD_1
	v_pk_add_f32 v[4:5], v[4:5], v[16:17]
	v_pk_add_f32 v[6:7], v[6:7], v[24:25]
	v_cvt_pk_f32_fp8_e32 v[16:17], v50
	v_cvt_pk_f32_fp8_sdwa v[24:25], v50 src0_sel:WORD_1
	v_pk_add_f32 v[8:9], v[8:9], v[16:17]
	v_pk_add_f32 v[10:11], v[10:11], v[24:25]
	v_cvt_pk_f32_fp8_e32 v[16:17], v51
	v_cvt_pk_f32_fp8_sdwa v[24:25], v51 src0_sel:WORD_1
	v_pk_add_f32 v[12:13], v[12:13], v[16:17]
	v_pk_add_f32 v[14:15], v[14:15], v[24:25]
	s_waitcnt vmcnt(2)
	v_cvt_pk_f32_fp8_e32 v[16:17], v52
	v_cvt_pk_f32_fp8_sdwa v[24:25], v52 src0_sel:WORD_1
	v_pk_add_f32 v[0:1], v[0:1], v[16:17]
	v_pk_add_f32 v[2:3], v[2:3], v[24:25]
	v_cvt_pk_f32_fp8_e32 v[16:17], v53
	v_cvt_pk_f32_fp8_sdwa v[24:25], v53 src0_sel:WORD_1
	v_pk_add_f32 v[4:5], v[4:5], v[16:17]
	v_pk_add_f32 v[6:7], v[6:7], v[24:25]
	v_cvt_pk_f32_fp8_e32 v[16:17], v54
	v_cvt_pk_f32_fp8_sdwa v[24:25], v54 src0_sel:WORD_1
	v_pk_add_f32 v[8:9], v[8:9], v[16:17]
	v_pk_add_f32 v[10:11], v[10:11], v[24:25]
	v_cvt_pk_f32_fp8_e32 v[16:17], v55
	v_cvt_pk_f32_fp8_sdwa v[24:25], v55 src0_sel:WORD_1
	v_pk_add_f32 v[12:13], v[12:13], v[16:17]
	v_pk_add_f32 v[14:15], v[14:15], v[24:25]
	s_waitcnt vmcnt(1)
	v_cvt_pk_f32_fp8_e32 v[16:17], v56
	v_cvt_pk_f32_fp8_sdwa v[24:25], v56 src0_sel:WORD_1
	v_pk_add_f32 v[0:1], v[0:1], v[16:17]
	v_pk_add_f32 v[2:3], v[2:3], v[24:25]
	v_cvt_pk_f32_fp8_e32 v[16:17], v57
	v_cvt_pk_f32_fp8_sdwa v[24:25], v57 src0_sel:WORD_1
	v_pk_add_f32 v[4:5], v[4:5], v[16:17]
	v_pk_add_f32 v[6:7], v[6:7], v[24:25]
	v_cvt_pk_f32_fp8_e32 v[16:17], v58
	v_cvt_pk_f32_fp8_sdwa v[24:25], v58 src0_sel:WORD_1
	v_pk_add_f32 v[8:9], v[8:9], v[16:17]
	v_pk_add_f32 v[10:11], v[10:11], v[24:25]
	v_cvt_pk_f32_fp8_e32 v[16:17], v59
	v_cvt_pk_f32_fp8_sdwa v[24:25], v59 src0_sel:WORD_1
	v_pk_add_f32 v[12:13], v[12:13], v[16:17]
	v_pk_add_f32 v[14:15], v[14:15], v[24:25]
	s_waitcnt vmcnt(0)
	v_cvt_pk_f32_fp8_e32 v[16:17], v60
	v_cvt_pk_f32_fp8_sdwa v[24:25], v60 src0_sel:WORD_1
	v_pk_add_f32 v[0:1], v[0:1], v[16:17]
	v_pk_add_f32 v[2:3], v[2:3], v[24:25]
	v_cvt_pk_f32_fp8_e32 v[16:17], v61
	v_cvt_pk_f32_fp8_sdwa v[24:25], v61 src0_sel:WORD_1
	v_pk_add_f32 v[4:5], v[4:5], v[16:17]
	v_pk_add_f32 v[6:7], v[6:7], v[24:25]
	v_cvt_pk_f32_fp8_e32 v[16:17], v62
	v_cvt_pk_f32_fp8_sdwa v[24:25], v62 src0_sel:WORD_1
	v_pk_add_f32 v[8:9], v[8:9], v[16:17]
	v_pk_add_f32 v[10:11], v[10:11], v[24:25]
	v_cvt_pk_f32_fp8_e32 v[16:17], v63
	v_cvt_pk_f32_fp8_sdwa v[24:25], v63 src0_sel:WORD_1
	v_pk_add_f32 v[12:13], v[12:13], v[16:17]
	v_pk_add_f32 v[14:15], v[14:15], v[24:25]
	v_add_u32_e32 v23, 0xffffffc4, v23
	v_add_u32_e32 v22, 0xf0, v22
	v_cmp_lt_i32_e64 s[58:59], 0, v23
	s_nop 1
	s_cmp_lg_u64 s[58:59], 0
	s_cbranch_scc1 .Lagg15_4

.LBB4_8:
	s_mov_b64 exec, -1
	s_nop 4
	v_add_f32_dpp v0, v0, v0 quad_perm:[1,0,3,2] row_mask:0xf bank_mask:0xf
	v_add_f32_dpp v1, v1, v1 quad_perm:[1,0,3,2] row_mask:0xf bank_mask:0xf
	v_add_f32_dpp v2, v2, v2 quad_perm:[1,0,3,2] row_mask:0xf bank_mask:0xf
	v_add_f32_dpp v3, v3, v3 quad_perm:[1,0,3,2] row_mask:0xf bank_mask:0xf
	v_add_f32_dpp v4, v4, v4 quad_perm:[1,0,3,2] row_mask:0xf bank_mask:0xf
	v_add_f32_dpp v5, v5, v5 quad_perm:[1,0,3,2] row_mask:0xf bank_mask:0xf
	v_add_f32_dpp v6, v6, v6 quad_perm:[1,0,3,2] row_mask:0xf bank_mask:0xf
	v_add_f32_dpp v7, v7, v7 quad_perm:[1,0,3,2] row_mask:0xf bank_mask:0xf
	v_add_f32_dpp v8, v8, v8 quad_perm:[1,0,3,2] row_mask:0xf bank_mask:0xf
	v_add_f32_dpp v9, v9, v9 quad_perm:[1,0,3,2] row_mask:0xf bank_mask:0xf
	v_add_f32_dpp v10, v10, v10 quad_perm:[1,0,3,2] row_mask:0xf bank_mask:0xf
	v_add_f32_dpp v11, v11, v11 quad_perm:[1,0,3,2] row_mask:0xf bank_mask:0xf
	v_add_f32_dpp v12, v12, v12 quad_perm:[1,0,3,2] row_mask:0xf bank_mask:0xf
	v_add_f32_dpp v13, v13, v13 quad_perm:[1,0,3,2] row_mask:0xf bank_mask:0xf
	v_add_f32_dpp v14, v14, v14 quad_perm:[1,0,3,2] row_mask:0xf bank_mask:0xf
	v_add_f32_dpp v15, v15, v15 quad_perm:[1,0,3,2] row_mask:0xf bank_mask:0xf
	v_add_f32_dpp v0, v0, v0 quad_perm:[2,3,0,1] row_mask:0xf bank_mask:0xf
	v_add_f32_dpp v1, v1, v1 quad_perm:[2,3,0,1] row_mask:0xf bank_mask:0xf
	v_add_f32_dpp v2, v2, v2 quad_perm:[2,3,0,1] row_mask:0xf bank_mask:0xf
	v_add_f32_dpp v3, v3, v3 quad_perm:[2,3,0,1] row_mask:0xf bank_mask:0xf
	v_add_f32_dpp v4, v4, v4 quad_perm:[2,3,0,1] row_mask:0xf bank_mask:0xf
	v_add_f32_dpp v5, v5, v5 quad_perm:[2,3,0,1] row_mask:0xf bank_mask:0xf
	v_add_f32_dpp v6, v6, v6 quad_perm:[2,3,0,1] row_mask:0xf bank_mask:0xf
	v_add_f32_dpp v7, v7, v7 quad_perm:[2,3,0,1] row_mask:0xf bank_mask:0xf
	v_add_f32_dpp v8, v8, v8 quad_perm:[2,3,0,1] row_mask:0xf bank_mask:0xf
	v_add_f32_dpp v9, v9, v9 quad_perm:[2,3,0,1] row_mask:0xf bank_mask:0xf
	v_add_f32_dpp v10, v10, v10 quad_perm:[2,3,0,1] row_mask:0xf bank_mask:0xf
	v_add_f32_dpp v11, v11, v11 quad_perm:[2,3,0,1] row_mask:0xf bank_mask:0xf
	v_add_f32_dpp v12, v12, v12 quad_perm:[2,3,0,1] row_mask:0xf bank_mask:0xf
	v_add_f32_dpp v13, v13, v13 quad_perm:[2,3,0,1] row_mask:0xf bank_mask:0xf
	v_add_f32_dpp v14, v14, v14 quad_perm:[2,3,0,1] row_mask:0xf bank_mask:0xf
	v_add_f32_dpp v15, v15, v15 quad_perm:[2,3,0,1] row_mask:0xf bank_mask:0xf
	s_and_b64 s[0:1], s[0:1], vcc
	s_and_saveexec_b64 s[2:3], s[0:1]
	s_cbranch_execz .LBB4_10
	s_waitcnt vmcnt(0) lgkmcnt(0)
	v_mul_f32_e32 v34, 0x3c800000, v34
	v_mul_f32_e32 v0, v34, v0
	v_mul_f32_e32 v1, v34, v1
	v_mul_f32_e32 v2, v34, v2
	v_mul_f32_e32 v3, v34, v3
	v_mul_f32_e32 v4, v34, v4
	v_mul_f32_e32 v5, v34, v5
	v_mul_f32_e32 v6, v34, v6
	v_mul_f32_e32 v7, v34, v7
	v_mul_f32_e32 v8, v34, v8
	v_mul_f32_e32 v9, v34, v9
	v_mul_f32_e32 v10, v34, v10
	v_mul_f32_e32 v11, v34, v11
	v_mul_f32_e32 v12, v34, v12
	v_mul_f32_e32 v13, v34, v13
	v_mul_f32_e32 v14, v34, v14
	v_mul_f32_e32 v15, v34, v15
	v_cvt_pk_f16_f32 v36, v0, v1
	v_cvt_pk_f16_f32 v37, v2, v3
	v_cvt_pk_f16_f32 v38, v4, v5
	v_cvt_pk_f16_f32 v39, v6, v7
	v_cvt_pk_f16_f32 v40, v8, v9
	v_cvt_pk_f16_f32 v41, v10, v11
	v_cvt_pk_f16_f32 v42, v12, v13
	v_cvt_pk_f16_f32 v43, v14, v15
	v_lshlrev_b64 v[16:17], 5, v[26:27]
	v_lshl_add_u64 v[16:17], s[12:13], 0, v[16:17]
	global_store_dwordx4 v[16:17], v[36:39], off
	global_store_dwordx4 v[16:17], v[40:43], off offset:16

	.amdhsa_kernel _Z5k_aggILi2EEvPKiS1_S1_PKDv4_jPKfS6_PS2_PDF16_
		.amdhsa_group_segment_fixed_size 0
		.amdhsa_private_segment_fixed_size 0
		.amdhsa_kernarg_size 64
		.amdhsa_user_sgpr_count 2
		.amdhsa_user_sgpr_dispatch_ptr 0
		.amdhsa_user_sgpr_queue_ptr 0
		.amdhsa_user_sgpr_kernarg_segment_ptr 1
		.amdhsa_user_sgpr_dispatch_id 0
		.amdhsa_user_sgpr_kernarg_preload_length 0
		.amdhsa_user_sgpr_kernarg_preload_offset 0
		.amdhsa_user_sgpr_private_segment_size 0
		.amdhsa_uses_dynamic_stack 0
		.amdhsa_enable_private_segment 0
		.amdhsa_system_sgpr_workgroup_id_x 1
		.amdhsa_system_sgpr_workgroup_id_y 0
		.amdhsa_system_sgpr_workgroup_id_z 0
		.amdhsa_system_sgpr_workgroup_info 0
		.amdhsa_system_vgpr_workitem_id 0
		.amdhsa_next_free_vgpr 72
		.amdhsa_next_free_sgpr 60
		.amdhsa_accum_offset 72
		.amdhsa_reserve_vcc 1
		.amdhsa_float_round_mode_32 0
		.amdhsa_float_round_mode_16_64 0
		.amdhsa_float_denorm_mode_32 3
		.amdhsa_float_denorm_mode_16_64 3
		.amdhsa_dx10_clamp 1
		.amdhsa_ieee_mode 1
		.amdhsa_fp16_overflow 0
		.amdhsa_tg_split 0
		.amdhsa_exception_fp_ieee_invalid_op 0
		.amdhsa_exception_fp_denorm_src 0
		.amdhsa_exception_fp_ieee_div_zero 0
		.amdhsa_exception_fp_ieee_overflow 0
		.amdhsa_exception_fp_ieee_underflow 0
		.amdhsa_exception_fp_ieee_inexact 0
		.amdhsa_exception_int_div_zero 0
	.end_amdhsa_kernel

amdhsa.kernels:
  - .agpr_count:     0
    .args:
      - .actual_access:  read_only
        .address_space:  global
        .offset:         0
        .size:           8
        .value_kind:     global_buffer
      - .actual_access:  read_only
        .address_space:  global
        .offset:         8
        .size:           8
        .value_kind:     global_buffer
      - .actual_access:  write_only
        .address_space:  global
        .offset:         16
        .size:           8
        .value_kind:     global_buffer
      - .actual_access:  read_only
        .address_space:  global
        .offset:         24
        .size:           8
        .value_kind:     global_buffer
      - .actual_access:  write_only
        .address_space:  global
        .offset:         32
        .size:           8
        .value_kind:     global_buffer
      - .actual_access:  write_only
        .address_space:  global
        .offset:         40
        .size:           8
        .value_kind:     global_buffer
      - .actual_access:  read_only
        .address_space:  global
        .offset:         48
        .size:           8
        .value_kind:     global_buffer
      - .actual_access:  read_only
        .address_space:  global
        .offset:         56
        .size:           8
        .value_kind:     global_buffer
      - .actual_access:  write_only
        .address_space:  global
        .offset:         64
        .size:           8
        .value_kind:     global_buffer
    .group_segment_fixed_size: 53904
    .kernarg_segment_align: 8
    .kernarg_segment_size: 72
    .language:       OpenCL C
    .language_version:
      - 2
      - 0
    .max_flat_workgroup_size: 1024
    .name:           _Z6k_partPKiS0_PiS1_PjS1_PKfS4_Pf
    .private_segment_fixed_size: 0
    .sgpr_count:     31
    .sgpr_spill_count: 0
    .symbol:         _Z6k_partPKiS0_PiS1_PjS1_PKfS4_Pf.kd
    .uniform_work_group_size: 1
    .uses_dynamic_stack: false
    .vgpr_count:     64
    .vgpr_spill_count: 0
    .wavefront_size: 64
  - .agpr_count:     0
    .args:
      - .actual_access:  read_only
        .address_space:  global
        .offset:         0
        .size:           8
        .value_kind:     global_buffer
      - .actual_access:  read_only
        .address_space:  global
        .offset:         8
        .size:           8
        .value_kind:     global_buffer
      - .actual_access:  read_only
        .address_space:  global
        .offset:         16
        .size:           8
        .value_kind:     global_buffer
      - .address_space:  global
        .offset:         24
        .size:           8
        .value_kind:     global_buffer
      - .actual_access:  read_only
        .address_space:  global
        .offset:         32
        .size:           8
        .value_kind:     global_buffer
      - .actual_access:  write_only
        .address_space:  global
        .offset:         40
        .size:           8
        .value_kind:     global_buffer
      - .actual_access:  write_only
        .address_space:  global
        .offset:         48
        .size:           8
        .value_kind:     global_buffer
      - .actual_access:  write_only
        .address_space:  global
        .offset:         56
        .size:           8
        .value_kind:     global_buffer
      - .actual_access:  write_only
        .address_space:  global
        .offset:         64
        .size:           8
        .value_kind:     global_buffer
      - .actual_access:  write_only
        .address_space:  global
        .offset:         72
        .size:           8
        .value_kind:     global_buffer
      - .actual_access:  read_only
        .address_space:  global
        .offset:         80
        .size:           8
        .value_kind:     global_buffer
      - .actual_access:  read_only
        .address_space:  global
        .offset:         88
        .size:           8
        .value_kind:     global_buffer
      - .actual_access:  read_only
        .address_space:  global
        .offset:         96
        .size:           8
        .value_kind:     global_buffer
      - .actual_access:  read_only
        .address_space:  global
        .offset:         104
        .size:           8
        .value_kind:     global_buffer
      - .actual_access:  write_only
        .address_space:  global
        .offset:         112
        .size:           8
        .value_kind:     global_buffer
      - .actual_access:  write_only
        .address_space:  global
        .offset:         120
        .size:           8
        .value_kind:     global_buffer
    .group_segment_fixed_size: 38940
    .kernarg_segment_align: 8
    .kernarg_segment_size: 128
    .language:       OpenCL C
    .language_version:
      - 2
      - 0
    .max_flat_workgroup_size: 1024
    .name:           _Z5k_csrPKjPKiS2_PiPKfPfPDF16_S3_S3_S3_S5_S5_S5_S5_S7_S6_
    .private_segment_fixed_size: 0
    .sgpr_count:     70
    .sgpr_spill_count: 0
    .symbol:         _Z5k_csrPKjPKiS2_PiPKfPfPDF16_S3_S3_S3_S5_S5_S5_S5_S7_S6_.kd
    .uniform_work_group_size: 1
    .uses_dynamic_stack: false
    .vgpr_count:     64
    .vgpr_spill_count: 0
    .wavefront_size: 64
  - .agpr_count:     0
    .args:
      - .actual_access:  read_only
        .address_space:  global
        .offset:         0
        .size:           8
        .value_kind:     global_buffer
      - .actual_access:  read_only
        .address_space:  global
        .offset:         8
        .size:           8
        .value_kind:     global_buffer
      - .actual_access:  read_only
        .address_space:  global
        .offset:         16
        .size:           8
        .value_kind:     global_buffer
      - .actual_access:  read_only
        .address_space:  global
        .offset:         24
        .size:           8
        .value_kind:     global_buffer
      - .actual_access:  read_only
        .address_space:  global
        .offset:         32
        .size:           8
        .value_kind:     global_buffer
      - .actual_access:  read_only
        .address_space:  global
        .offset:         40
        .size:           8
        .value_kind:     global_buffer
      - .actual_access:  write_only
        .address_space:  global
        .offset:         48
        .size:           8
        .value_kind:     global_buffer
      - .offset:         56
        .size:           4
        .value_kind:     hidden_block_count_x
      - .offset:         60
        .size:           4
        .value_kind:     hidden_block_count_y
      - .offset:         64
        .size:           4
        .value_kind:     hidden_block_count_z
      - .offset:         68
        .size:           2
        .value_kind:     hidden_group_size_x
      - .offset:         70
        .size:           2
        .value_kind:     hidden_group_size_y
      - .offset:         72
        .size:           2
        .value_kind:     hidden_group_size_z
      - .offset:         74
        .size:           2
        .value_kind:     hidden_remainder_x
      - .offset:         76
        .size:           2
        .value_kind:     hidden_remainder_y
      - .offset:         78
        .size:           2
        .value_kind:     hidden_remainder_z
      - .offset:         96
        .size:           8
        .value_kind:     hidden_global_offset_x
      - .offset:         104
        .size:           8
        .value_kind:     hidden_global_offset_y
      - .offset:         112
        .size:           8
        .value_kind:     hidden_global_offset_z
      - .offset:         120
        .size:           2
        .value_kind:     hidden_grid_dims
    .group_segment_fixed_size: 32768
    .kernarg_segment_align: 8
    .kernarg_segment_size: 312
    .language:       OpenCL C
    .language_version:
      - 2
      - 0
    .max_flat_workgroup_size: 256
    .name:           _Z5k_decPKiPKDF16_S2_PKfS4_S4_Pf
    .private_segment_fixed_size: 0
    .sgpr_count:     28
    .sgpr_spill_count: 0
    .symbol:         _Z5k_decPKiPKDF16_S2_PKfS4_S4_Pf.kd
    .uniform_work_group_size: 1
    .uses_dynamic_stack: false
    .vgpr_count:     248
    .vgpr_spill_count: 0
    .wavefront_size: 64
  - .agpr_count:     0
    .args:
      - .actual_access:  read_only
        .address_space:  global
        .offset:         0
        .size:           8
        .value_kind:     global_buffer
      - .actual_access:  read_only
        .address_space:  global
        .offset:         8
        .size:           8
        .value_kind:     global_buffer
      - .actual_access:  read_only
        .address_space:  global
        .offset:         16
        .size:           8
        .value_kind:     global_buffer
      - .actual_access:  read_only
        .address_space:  global
        .offset:         24
        .size:           8
        .value_kind:     global_buffer
      - .actual_access:  read_only
        .address_space:  global
        .offset:         32
        .size:           8
        .value_kind:     global_buffer
      - .actual_access:  read_only
        .address_space:  global
        .offset:         40
        .size:           8
        .value_kind:     global_buffer
      - .actual_access:  write_only
        .address_space:  global
        .offset:         48
        .size:           8
        .value_kind:     global_buffer
      - .actual_access:  read_only
        .address_space:  global
        .offset:         56
        .size:           8
        .value_kind:     global_buffer
    .group_segment_fixed_size: 0
    .kernarg_segment_align: 8
    .kernarg_segment_size: 64
    .language:       OpenCL C
    .language_version:
      - 2
      - 0
    .max_flat_workgroup_size: 64
    .name:           _Z5k_aggILi1EEvPKiS1_S1_PKDv4_jPKfS6_PS2_PDF16_
    .private_segment_fixed_size: 0
    .sgpr_count:     82
    .sgpr_spill_count: 0
    .symbol:         _Z5k_aggILi1EEvPKiS1_S1_PKDv4_jPKfS6_PS2_PDF16_.kd
    .uniform_work_group_size: 1
    .uses_dynamic_stack: false
    .vgpr_count:     72
    .vgpr_spill_count: 0
    .wavefront_size: 64
  - .agpr_count:     0
    .args:
      - .actual_access:  read_only
        .address_space:  global
        .offset:         0
        .size:           8
        .value_kind:     global_buffer
      - .actual_access:  read_only
        .address_space:  global
        .offset:         8
        .size:           8
        .value_kind:     global_buffer
      - .actual_access:  read_only
        .address_space:  global
        .offset:         16
        .size:           8
        .value_kind:     global_buffer
      - .actual_access:  read_only
        .address_space:  global
        .offset:         24
        .size:           8
        .value_kind:     global_buffer
      - .actual_access:  read_only
        .address_space:  global
        .offset:         32
        .size:           8
        .value_kind:     global_buffer
      - .actual_access:  read_only
        .address_space:  global
        .offset:         40
        .size:           8
        .value_kind:     global_buffer
      - .actual_access:  read_only
        .address_space:  global
        .offset:         48
        .size:           8
        .value_kind:     global_buffer
      - .actual_access:  write_only
        .address_space:  global
        .offset:         56
        .size:           8
        .value_kind:     global_buffer
    .group_segment_fixed_size: 0
    .kernarg_segment_align: 8
    .kernarg_segment_size: 64
    .language:       OpenCL C
    .language_version:
      - 2
      - 0
    .max_flat_workgroup_size: 64
    .name:           _Z5k_aggILi2EEvPKiS1_S1_PKDv4_jPKfS6_PS2_PDF16_
    .private_segment_fixed_size: 0
    .sgpr_count:     66
    .sgpr_spill_count: 0
    .symbol:         _Z5k_aggILi2EEvPKiS1_S1_PKDv4_jPKfS6_PS2_PDF16_.kd
    .uniform_work_group_size: 1
    .uses_dynamic_stack: false
    .vgpr_count:     72
    .vgpr_spill_count: 0
    .wavefront_size: 64
